# baseline (speedup 1.0000x reference)
_Z12k1_colsum_q8PKfPjPfS2_:
	s_load_dwordx8 s[4:11], s[0:1], 0x0
	v_and_b32_e32 v1, 63, v0
	v_lshrrev_b32_e32 v41, 6, v0
	s_mul_i32 s12, s2, 0xc35
	s_lshr_b32 s12, s12, 4
	v_readfirstlane_b32 s14, v41
	s_add_i32 s13, s2, 1
	s_mul_i32 s13, s13, 0xc35
	s_lshr_b32 s13, s13, 4
	s_sub_u32 s13, s13, s12
	s_sub_u32 s15, s13, 0xc0
	s_cmp_lt_u32 s14, s15
	s_cselect_b32 s29, 1, 0
	v_lshlrev_b32_e32 v34, 4, v1
	v_min_u32_e32 v35, 57, v1
	v_lshlrev_b32_e32 v35, 4, v35
	v_cmp_gt_u32_e64 s[18:19], 58, v1
	s_lshl_b32 s35, s14, 13
	s_add_u32 s36, s35, 0x1000
	v_add_u32_e32 v38, s35, v34
	v_lshrrev_b32_e32 v41, 5, v1
	v_mov_b32_e32 v42, 0xc35000
	v_mul_lo_u32 v39, v41, v42
	v_and_b32_e32 v42, 31, v1
	v_lshl_add_u32 v39, v42, 2, v39
	v_mov_b32_e32 v2, 0
	v_mov_b32_e32 v3, 0
	v_mov_b32_e32 v4, 0
	v_mov_b32_e32 v5, 0
	v_mov_b32_e32 v6, 0
	v_mov_b32_e32 v7, 0
	v_mov_b32_e32 v8, 0
	v_mov_b32_e32 v9, 0
	v_mov_b32_e32 v10, 0
	v_mov_b32_e32 v11, 0
	v_mov_b32_e32 v12, 0
	v_mov_b32_e32 v13, 0
	v_mov_b32_e32 v14, 0
	v_mov_b32_e32 v15, 0
	v_mov_b32_e32 v16, 0
	v_mov_b32_e32 v17, 0
	v_mov_b32_e32 v40, 0
	v_mov_b32_e32 v47, 0x42fe0000
	s_mov_b32 s32, 0x42fe0000
	s_mov_b32 s33, 0xc0c0400
	s_mov_b32 s34, 0x4000c0c
	s_add_u32 s15, s12, s14
	s_mul_i32 s37, s15, 0xfa0
	s_lshl_b32 s15, s15, 7
	s_waitcnt lgkmcnt(0)
	s_add_u32 s16, s4, s37
	s_addc_u32 s17, s5, 0
	s_add_u32 s40, s6, s15
	s_addc_u32 s41, s7, 0
	s_add_u32 s20, s40, 0
	s_addc_u32 s21, s41, 0
	s_add_u32 s22, s20, 0x186a000
	s_addc_u32 s23, s21, 0
	s_add_u32 s24, s22, 0x186a000
	s_addc_u32 s25, s23, 0
	s_add_u32 s26, s24, 0x186a000
	s_addc_u32 s27, s25, 0
	s_mov_b32 m0, s35
	s_nop 0
	global_load_lds_dwordx4 v34, s[16:17] nt
	global_load_lds_dwordx4 v34, s[16:17] offset:1024 nt
	global_load_lds_dwordx4 v34, s[16:17] offset:2048 nt
	global_load_lds_dwordx4 v35, s[16:17] offset:3072 nt
	s_add_u32 s16, s16, 0x7d00
	s_addc_u32 s17, s17, 0
	s_waitcnt vmcnt(0)
	ds_read_b128 v[18:21], v38 offset:0
	ds_read_b128 v[22:25], v38 offset:1024
	ds_read_b128 v[26:29], v38 offset:2048
	ds_read_b128 v[30:33], v38 offset:3072
	s_waitcnt lgkmcnt(0)
	s_barrier
	s_mov_b32 m0, s35
	s_nop 0
	global_load_lds_dwordx4 v34, s[16:17] nt
	global_load_lds_dwordx4 v34, s[16:17] offset:1024 nt
	global_load_lds_dwordx4 v34, s[16:17] offset:2048 nt
	global_load_lds_dwordx4 v35, s[16:17] offset:3072 nt
	s_add_u32 s16, s16, 0x7d00
	s_addc_u32 s17, s17, 0
	v_cndmask_b32_e64 v30, 0, v30, s[18:19]
	v_cndmask_b32_e64 v31, 0, v31, s[18:19]
	v_cndmask_b32_e64 v32, 0, v32, s[18:19]
	v_cndmask_b32_e64 v33, 0, v33, s[18:19]
	v_max3_f32 v41, |v18|, |v19|, |v20|
	v_max3_f32 v42, |v21|, |v22|, |v23|
	v_max3_f32 v43, |v24|, |v25|, |v26|
	v_max3_f32 v44, |v27|, |v28|, |v29|
	v_max3_f32 v48, |v30|, |v31|, |v32|
	v_max3_f32 v41, v41, v42, |v33|
	v_max3_f32 v43, v43, v44, v48
	v_max_f32_e32 v41, v41, v43
	v_pk_add_f32 v[2:3], v[2:3], v[18:19]
	v_pk_add_f32 v[4:5], v[4:5], v[20:21]
	v_max_f32_dpp v41, v41, v41 quad_perm:[1,0,3,2] row_mask:0xf bank_mask:0xf
	v_pk_add_f32 v[6:7], v[6:7], v[22:23]
	v_pk_add_f32 v[8:9], v[8:9], v[24:25]
	v_max_f32_dpp v41, v41, v41 quad_perm:[2,3,0,1] row_mask:0xf bank_mask:0xf
	v_pk_add_f32 v[10:11], v[10:11], v[26:27]
	v_pk_add_f32 v[12:13], v[12:13], v[28:29]
	v_max_f32_dpp v41, v41, v41 row_half_mirror row_mask:0xf bank_mask:0xf
	v_pk_add_f32 v[14:15], v[14:15], v[30:31]
	v_pk_add_f32 v[16:17], v[16:17], v[32:33]
	v_max_f32_dpp v41, v41, v41 row_mirror row_mask:0xf bank_mask:0xf
	s_nop 1
	v_max_f32_dpp v41, v41, v41 row_bcast:15 row_mask:0xa bank_mask:0xf
	s_nop 1
	v_max_f32_dpp v41, v41, v41 row_bcast:31 row_mask:0xc bank_mask:0xf
	s_nop 1
	v_readlane_b32 s28, v41, 63
	s_nop 1
	v_div_scale_f32 v48, s[30:31], s28, s28, v47
	v_rcp_f32_e32 v49, v48
	s_nop 0
	v_fma_f32 v50, -v48, v49, 1.0
	v_fmac_f32_e32 v49, v50, v49
	v_mov_b32_e32 v50, s28
	v_div_scale_f32 v50, vcc, s32, v50, s32
	v_mul_f32_e32 v51, v50, v49
	v_fma_f32 v52, -v48, v51, v50
	v_fmac_f32_e32 v51, v52, v49
	v_fma_f32 v48, -v48, v51, v50
	v_div_fmas_f32 v48, v48, v49, v51
	v_div_fixup_f32 v48, v48, s28, v47
	v_cmp_gt_f32_e64 vcc, s28, 0
	v_writelane_b32 v40, s28, 0
	s_nop 0
	v_cndmask_b32_e32 v48, 0, v48, vcc
	v_fmaak_f32 v49, v18, v48, 0x4b400000
	v_fmaak_f32 v50, v19, v48, 0x4b400000
	v_fmaak_f32 v51, v20, v48, 0x4b400000
	v_fmaak_f32 v52, v21, v48, 0x4b400000
	v_perm_b32 v49, v50, v49, s33
	v_perm_b32 v51, v52, v51, s34
	v_or_b32_e32 v56, v49, v51
	v_fmaak_f32 v41, v22, v48, 0x4b400000
	v_fmaak_f32 v42, v23, v48, 0x4b400000
	v_fmaak_f32 v43, v24, v48, 0x4b400000
	v_fmaak_f32 v44, v25, v48, 0x4b400000
	v_perm_b32 v41, v42, v41, s33
	v_perm_b32 v43, v44, v43, s34
	v_or_b32_e32 v57, v41, v43
	v_fmaak_f32 v49, v26, v48, 0x4b400000
	v_fmaak_f32 v50, v27, v48, 0x4b400000
	v_fmaak_f32 v51, v28, v48, 0x4b400000
	v_fmaak_f32 v52, v29, v48, 0x4b400000
	v_perm_b32 v49, v50, v49, s33
	v_perm_b32 v51, v52, v51, s34
	v_or_b32_e32 v58, v49, v51
	v_fmaak_f32 v41, v30, v48, 0x4b400000
	v_fmaak_f32 v42, v31, v48, 0x4b400000
	v_fmaak_f32 v43, v32, v48, 0x4b400000
	v_fmaak_f32 v44, v33, v48, 0x4b400000
	v_perm_b32 v41, v42, v41, s33
	v_perm_b32 v43, v44, v43, s34
	v_or_b32_e32 v59, v41, v43
	s_waitcnt vmcnt(0)
	ds_read_b128 v[18:21], v38 offset:0
	ds_read_b128 v[22:25], v38 offset:1024
	ds_read_b128 v[26:29], v38 offset:2048
	ds_read_b128 v[30:33], v38 offset:3072
	s_waitcnt lgkmcnt(0)
	s_barrier
	s_mov_b32 m0, s35
	s_nop 0
	global_load_lds_dwordx4 v34, s[16:17] nt
	global_load_lds_dwordx4 v34, s[16:17] offset:1024 nt
	global_load_lds_dwordx4 v34, s[16:17] offset:2048 nt
	global_load_lds_dwordx4 v35, s[16:17] offset:3072 nt
	s_add_u32 s16, s16, 0x7d00
	s_addc_u32 s17, s17, 0
	v_cndmask_b32_e64 v30, 0, v30, s[18:19]
	v_cndmask_b32_e64 v31, 0, v31, s[18:19]
	v_cndmask_b32_e64 v32, 0, v32, s[18:19]
	v_cndmask_b32_e64 v33, 0, v33, s[18:19]
	v_max3_f32 v41, |v18|, |v19|, |v20|
	v_max3_f32 v42, |v21|, |v22|, |v23|
	v_max3_f32 v43, |v24|, |v25|, |v26|
	v_max3_f32 v44, |v27|, |v28|, |v29|
	v_max3_f32 v48, |v30|, |v31|, |v32|
	v_max3_f32 v41, v41, v42, |v33|
	v_max3_f32 v43, v43, v44, v48
	v_max_f32_e32 v41, v41, v43
	v_pk_add_f32 v[2:3], v[2:3], v[18:19]
	v_pk_add_f32 v[4:5], v[4:5], v[20:21]
	v_max_f32_dpp v41, v41, v41 quad_perm:[1,0,3,2] row_mask:0xf bank_mask:0xf
	v_pk_add_f32 v[6:7], v[6:7], v[22:23]
	v_pk_add_f32 v[8:9], v[8:9], v[24:25]
	v_max_f32_dpp v41, v41, v41 quad_perm:[2,3,0,1] row_mask:0xf bank_mask:0xf
	v_pk_add_f32 v[10:11], v[10:11], v[26:27]
	v_pk_add_f32 v[12:13], v[12:13], v[28:29]
	v_max_f32_dpp v41, v41, v41 row_half_mirror row_mask:0xf bank_mask:0xf
	v_pk_add_f32 v[14:15], v[14:15], v[30:31]
	v_pk_add_f32 v[16:17], v[16:17], v[32:33]
	v_max_f32_dpp v41, v41, v41 row_mirror row_mask:0xf bank_mask:0xf
	s_nop 1
	v_max_f32_dpp v41, v41, v41 row_bcast:15 row_mask:0xa bank_mask:0xf
	s_nop 1
	v_max_f32_dpp v41, v41, v41 row_bcast:31 row_mask:0xc bank_mask:0xf
	s_nop 1
	v_readlane_b32 s28, v41, 63
	s_nop 1
	v_div_scale_f32 v48, s[30:31], s28, s28, v47
	v_rcp_f32_e32 v49, v48
	s_nop 0
	v_fma_f32 v50, -v48, v49, 1.0
	v_fmac_f32_e32 v49, v50, v49
	v_mov_b32_e32 v50, s28
	v_div_scale_f32 v50, vcc, s32, v50, s32
	v_mul_f32_e32 v51, v50, v49
	v_fma_f32 v52, -v48, v51, v50
	v_fmac_f32_e32 v51, v52, v49
	v_fma_f32 v48, -v48, v51, v50
	v_div_fmas_f32 v48, v48, v49, v51
	v_div_fixup_f32 v48, v48, s28, v47
	v_cmp_gt_f32_e64 vcc, s28, 0
	v_writelane_b32 v40, s28, 1
	s_nop 0
	v_cndmask_b32_e32 v48, 0, v48, vcc
	v_fmaak_f32 v49, v18, v48, 0x4b400000
	v_fmaak_f32 v50, v19, v48, 0x4b400000
	v_fmaak_f32 v51, v20, v48, 0x4b400000
	v_fmaak_f32 v52, v21, v48, 0x4b400000
	v_perm_b32 v49, v50, v49, s33
	v_perm_b32 v51, v52, v51, s34
	v_or_b32_e32 v60, v49, v51
	v_fmaak_f32 v41, v22, v48, 0x4b400000
	v_fmaak_f32 v42, v23, v48, 0x4b400000
	v_fmaak_f32 v43, v24, v48, 0x4b400000
	v_fmaak_f32 v44, v25, v48, 0x4b400000
	v_perm_b32 v41, v42, v41, s33
	v_perm_b32 v43, v44, v43, s34
	v_or_b32_e32 v61, v41, v43
	v_fmaak_f32 v49, v26, v48, 0x4b400000
	v_fmaak_f32 v50, v27, v48, 0x4b400000
	v_fmaak_f32 v51, v28, v48, 0x4b400000
	v_fmaak_f32 v52, v29, v48, 0x4b400000
	v_perm_b32 v49, v50, v49, s33
	v_perm_b32 v51, v52, v51, s34
	v_or_b32_e32 v62, v49, v51
	v_fmaak_f32 v41, v30, v48, 0x4b400000
	v_fmaak_f32 v42, v31, v48, 0x4b400000
	v_fmaak_f32 v43, v32, v48, 0x4b400000
	v_fmaak_f32 v44, v33, v48, 0x4b400000
	v_perm_b32 v41, v42, v41, s33
	v_perm_b32 v43, v44, v43, s34
	v_or_b32_e32 v63, v41, v43
	s_waitcnt vmcnt(0)
	ds_read_b128 v[18:21], v38 offset:0
	ds_read_b128 v[22:25], v38 offset:1024
	ds_read_b128 v[26:29], v38 offset:2048
	ds_read_b128 v[30:33], v38 offset:3072
	s_waitcnt lgkmcnt(0)
	s_barrier
	s_mov_b32 m0, s35
	s_nop 0
	global_load_lds_dwordx4 v34, s[16:17] nt
	global_load_lds_dwordx4 v34, s[16:17] offset:1024 nt
	global_load_lds_dwordx4 v34, s[16:17] offset:2048 nt
	global_load_lds_dwordx4 v35, s[16:17] offset:3072 nt
	s_add_u32 s16, s16, 0x7d00
	s_addc_u32 s17, s17, 0
	v_cndmask_b32_e64 v30, 0, v30, s[18:19]
	v_cndmask_b32_e64 v31, 0, v31, s[18:19]
	v_cndmask_b32_e64 v32, 0, v32, s[18:19]
	v_cndmask_b32_e64 v33, 0, v33, s[18:19]
	v_max3_f32 v41, |v18|, |v19|, |v20|
	v_max3_f32 v42, |v21|, |v22|, |v23|
	v_max3_f32 v43, |v24|, |v25|, |v26|
	v_max3_f32 v44, |v27|, |v28|, |v29|
	v_max3_f32 v48, |v30|, |v31|, |v32|
	v_max3_f32 v41, v41, v42, |v33|
	v_max3_f32 v43, v43, v44, v48
	v_max_f32_e32 v41, v41, v43
	v_pk_add_f32 v[2:3], v[2:3], v[18:19]
	v_pk_add_f32 v[4:5], v[4:5], v[20:21]
	v_max_f32_dpp v41, v41, v41 quad_perm:[1,0,3,2] row_mask:0xf bank_mask:0xf
	v_pk_add_f32 v[6:7], v[6:7], v[22:23]
	v_pk_add_f32 v[8:9], v[8:9], v[24:25]
	v_max_f32_dpp v41, v41, v41 quad_perm:[2,3,0,1] row_mask:0xf bank_mask:0xf
	v_pk_add_f32 v[10:11], v[10:11], v[26:27]
	v_pk_add_f32 v[12:13], v[12:13], v[28:29]
	v_max_f32_dpp v41, v41, v41 row_half_mirror row_mask:0xf bank_mask:0xf
	v_pk_add_f32 v[14:15], v[14:15], v[30:31]
	v_pk_add_f32 v[16:17], v[16:17], v[32:33]
	v_max_f32_dpp v41, v41, v41 row_mirror row_mask:0xf bank_mask:0xf
	s_nop 1
	v_max_f32_dpp v41, v41, v41 row_bcast:15 row_mask:0xa bank_mask:0xf
	s_nop 1
	v_max_f32_dpp v41, v41, v41 row_bcast:31 row_mask:0xc bank_mask:0xf
	s_nop 1
	v_readlane_b32 s28, v41, 63
	s_nop 1
	v_div_scale_f32 v48, s[30:31], s28, s28, v47
	v_rcp_f32_e32 v49, v48
	s_nop 0
	v_fma_f32 v50, -v48, v49, 1.0
	v_fmac_f32_e32 v49, v50, v49
	v_mov_b32_e32 v50, s28
	v_div_scale_f32 v50, vcc, s32, v50, s32
	v_mul_f32_e32 v51, v50, v49
	v_fma_f32 v52, -v48, v51, v50
	v_fmac_f32_e32 v51, v52, v49
	v_fma_f32 v48, -v48, v51, v50
	v_div_fmas_f32 v48, v48, v49, v51
	v_div_fixup_f32 v48, v48, s28, v47
	v_cmp_gt_f32_e64 vcc, s28, 0
	v_writelane_b32 v40, s28, 2
	s_nop 0
	v_cndmask_b32_e32 v48, 0, v48, vcc
	v_fmaak_f32 v49, v18, v48, 0x4b400000
	v_fmaak_f32 v50, v19, v48, 0x4b400000
	v_fmaak_f32 v51, v20, v48, 0x4b400000
	v_fmaak_f32 v52, v21, v48, 0x4b400000
	v_perm_b32 v49, v50, v49, s33
	v_perm_b32 v51, v52, v51, s34
	v_or_b32_e32 v64, v49, v51
	v_fmaak_f32 v41, v22, v48, 0x4b400000
	v_fmaak_f32 v42, v23, v48, 0x4b400000
	v_fmaak_f32 v43, v24, v48, 0x4b400000
	v_fmaak_f32 v44, v25, v48, 0x4b400000
	v_perm_b32 v41, v42, v41, s33
	v_perm_b32 v43, v44, v43, s34
	v_or_b32_e32 v65, v41, v43
	v_fmaak_f32 v49, v26, v48, 0x4b400000
	v_fmaak_f32 v50, v27, v48, 0x4b400000
	v_fmaak_f32 v51, v28, v48, 0x4b400000
	v_fmaak_f32 v52, v29, v48, 0x4b400000
	v_perm_b32 v49, v50, v49, s33
	v_perm_b32 v51, v52, v51, s34
	v_or_b32_e32 v66, v49, v51
	v_fmaak_f32 v41, v30, v48, 0x4b400000
	v_fmaak_f32 v42, v31, v48, 0x4b400000
	v_fmaak_f32 v43, v32, v48, 0x4b400000
	v_fmaak_f32 v44, v33, v48, 0x4b400000
	v_perm_b32 v41, v42, v41, s33
	v_perm_b32 v43, v44, v43, s34
	v_or_b32_e32 v67, v41, v43
	s_waitcnt vmcnt(0)
	ds_read_b128 v[18:21], v38 offset:0
	ds_read_b128 v[22:25], v38 offset:1024
	ds_read_b128 v[26:29], v38 offset:2048
	ds_read_b128 v[30:33], v38 offset:3072
	s_waitcnt lgkmcnt(0)
	s_barrier
	s_mov_b32 m0, s35
	s_nop 0
	global_load_lds_dwordx4 v34, s[16:17] nt
	global_load_lds_dwordx4 v34, s[16:17] offset:1024 nt
	global_load_lds_dwordx4 v34, s[16:17] offset:2048 nt
	global_load_lds_dwordx4 v35, s[16:17] offset:3072 nt
	s_add_u32 s16, s16, 0x7d00
	s_addc_u32 s17, s17, 0
	v_cndmask_b32_e64 v30, 0, v30, s[18:19]
	v_cndmask_b32_e64 v31, 0, v31, s[18:19]
	v_cndmask_b32_e64 v32, 0, v32, s[18:19]
	v_cndmask_b32_e64 v33, 0, v33, s[18:19]
	v_max3_f32 v41, |v18|, |v19|, |v20|
	v_max3_f32 v42, |v21|, |v22|, |v23|
	v_max3_f32 v43, |v24|, |v25|, |v26|
	v_max3_f32 v44, |v27|, |v28|, |v29|
	v_max3_f32 v48, |v30|, |v31|, |v32|
	v_max3_f32 v41, v41, v42, |v33|
	v_max3_f32 v43, v43, v44, v48
	v_max_f32_e32 v41, v41, v43
	v_pk_add_f32 v[2:3], v[2:3], v[18:19]
	v_pk_add_f32 v[4:5], v[4:5], v[20:21]
	v_max_f32_dpp v41, v41, v41 quad_perm:[1,0,3,2] row_mask:0xf bank_mask:0xf
	v_pk_add_f32 v[6:7], v[6:7], v[22:23]
	v_pk_add_f32 v[8:9], v[8:9], v[24:25]
	v_max_f32_dpp v41, v41, v41 quad_perm:[2,3,0,1] row_mask:0xf bank_mask:0xf
	v_pk_add_f32 v[10:11], v[10:11], v[26:27]
	v_pk_add_f32 v[12:13], v[12:13], v[28:29]
	v_max_f32_dpp v41, v41, v41 row_half_mirror row_mask:0xf bank_mask:0xf
	v_pk_add_f32 v[14:15], v[14:15], v[30:31]
	v_pk_add_f32 v[16:17], v[16:17], v[32:33]
	v_max_f32_dpp v41, v41, v41 row_mirror row_mask:0xf bank_mask:0xf
	s_nop 1
	v_max_f32_dpp v41, v41, v41 row_bcast:15 row_mask:0xa bank_mask:0xf
	s_nop 1
	v_max_f32_dpp v41, v41, v41 row_bcast:31 row_mask:0xc bank_mask:0xf
	s_nop 1
	v_readlane_b32 s28, v41, 63
	s_nop 1
	v_div_scale_f32 v48, s[30:31], s28, s28, v47
	v_rcp_f32_e32 v49, v48
	s_nop 0
	v_fma_f32 v50, -v48, v49, 1.0
	v_fmac_f32_e32 v49, v50, v49
	v_mov_b32_e32 v50, s28
	v_div_scale_f32 v50, vcc, s32, v50, s32
	v_mul_f32_e32 v51, v50, v49
	v_fma_f32 v52, -v48, v51, v50
	v_fmac_f32_e32 v51, v52, v49
	v_fma_f32 v48, -v48, v51, v50
	v_div_fmas_f32 v48, v48, v49, v51
	v_div_fixup_f32 v48, v48, s28, v47
	v_cmp_gt_f32_e64 vcc, s28, 0
	v_writelane_b32 v40, s28, 3
	s_nop 0
	v_cndmask_b32_e32 v48, 0, v48, vcc
	v_fmaak_f32 v49, v18, v48, 0x4b400000
	v_fmaak_f32 v50, v19, v48, 0x4b400000
	v_fmaak_f32 v51, v20, v48, 0x4b400000
	v_fmaak_f32 v52, v21, v48, 0x4b400000
	v_perm_b32 v49, v50, v49, s33
	v_perm_b32 v51, v52, v51, s34
	v_or_b32_e32 v68, v49, v51
	v_fmaak_f32 v41, v22, v48, 0x4b400000
	v_fmaak_f32 v42, v23, v48, 0x4b400000
	v_fmaak_f32 v43, v24, v48, 0x4b400000
	v_fmaak_f32 v44, v25, v48, 0x4b400000
	v_perm_b32 v41, v42, v41, s33
	v_perm_b32 v43, v44, v43, s34
	v_or_b32_e32 v69, v41, v43
	v_fmaak_f32 v49, v26, v48, 0x4b400000
	v_fmaak_f32 v50, v27, v48, 0x4b400000
	v_fmaak_f32 v51, v28, v48, 0x4b400000
	v_fmaak_f32 v52, v29, v48, 0x4b400000
	v_perm_b32 v49, v50, v49, s33
	v_perm_b32 v51, v52, v51, s34
	v_or_b32_e32 v70, v49, v51
	v_fmaak_f32 v41, v30, v48, 0x4b400000
	v_fmaak_f32 v42, v31, v48, 0x4b400000
	v_fmaak_f32 v43, v32, v48, 0x4b400000
	v_fmaak_f32 v44, v33, v48, 0x4b400000
	v_perm_b32 v41, v42, v41, s33
	v_perm_b32 v43, v44, v43, s34
	v_or_b32_e32 v71, v41, v43
	s_waitcnt vmcnt(0)
	ds_read_b128 v[18:21], v38 offset:0
	ds_read_b128 v[22:25], v38 offset:1024
	ds_read_b128 v[26:29], v38 offset:2048
	ds_read_b128 v[30:33], v38 offset:3072
	s_waitcnt lgkmcnt(0)
	s_barrier
	s_mov_b32 m0, s35
	s_nop 0
	global_load_lds_dwordx4 v34, s[16:17] nt
	global_load_lds_dwordx4 v34, s[16:17] offset:1024 nt
	global_load_lds_dwordx4 v34, s[16:17] offset:2048 nt
	global_load_lds_dwordx4 v35, s[16:17] offset:3072 nt
	s_add_u32 s16, s16, 0x7d00
	s_addc_u32 s17, s17, 0
	v_cndmask_b32_e64 v30, 0, v30, s[18:19]
	v_cndmask_b32_e64 v31, 0, v31, s[18:19]
	v_cndmask_b32_e64 v32, 0, v32, s[18:19]
	v_cndmask_b32_e64 v33, 0, v33, s[18:19]
	v_max3_f32 v41, |v18|, |v19|, |v20|
	v_max3_f32 v42, |v21|, |v22|, |v23|
	v_max3_f32 v43, |v24|, |v25|, |v26|
	v_max3_f32 v44, |v27|, |v28|, |v29|
	v_max3_f32 v48, |v30|, |v31|, |v32|
	v_max3_f32 v41, v41, v42, |v33|
	v_max3_f32 v43, v43, v44, v48
	v_max_f32_e32 v41, v41, v43
	v_pk_add_f32 v[2:3], v[2:3], v[18:19]
	v_pk_add_f32 v[4:5], v[4:5], v[20:21]
	v_max_f32_dpp v41, v41, v41 quad_perm:[1,0,3,2] row_mask:0xf bank_mask:0xf
	v_pk_add_f32 v[6:7], v[6:7], v[22:23]
	v_pk_add_f32 v[8:9], v[8:9], v[24:25]
	v_max_f32_dpp v41, v41, v41 quad_perm:[2,3,0,1] row_mask:0xf bank_mask:0xf
	v_pk_add_f32 v[10:11], v[10:11], v[26:27]
	v_pk_add_f32 v[12:13], v[12:13], v[28:29]
	v_max_f32_dpp v41, v41, v41 row_half_mirror row_mask:0xf bank_mask:0xf
	v_pk_add_f32 v[14:15], v[14:15], v[30:31]
	v_pk_add_f32 v[16:17], v[16:17], v[32:33]
	v_max_f32_dpp v41, v41, v41 row_mirror row_mask:0xf bank_mask:0xf
	s_nop 1
	v_max_f32_dpp v41, v41, v41 row_bcast:15 row_mask:0xa bank_mask:0xf
	s_nop 1
	v_max_f32_dpp v41, v41, v41 row_bcast:31 row_mask:0xc bank_mask:0xf
	s_nop 1
	v_readlane_b32 s28, v41, 63
	s_nop 1
	v_div_scale_f32 v48, s[30:31], s28, s28, v47
	v_rcp_f32_e32 v49, v48
	s_nop 0
	v_fma_f32 v50, -v48, v49, 1.0
	v_fmac_f32_e32 v49, v50, v49
	v_mov_b32_e32 v50, s28
	v_div_scale_f32 v50, vcc, s32, v50, s32
	v_mul_f32_e32 v51, v50, v49
	v_fma_f32 v52, -v48, v51, v50
	v_fmac_f32_e32 v51, v52, v49
	v_fma_f32 v48, -v48, v51, v50
	v_div_fmas_f32 v48, v48, v49, v51
	v_div_fixup_f32 v48, v48, s28, v47
	v_cmp_gt_f32_e64 vcc, s28, 0
	v_writelane_b32 v40, s28, 4
	s_nop 0
	v_cndmask_b32_e32 v48, 0, v48, vcc
	v_fmaak_f32 v49, v18, v48, 0x4b400000
	v_fmaak_f32 v50, v19, v48, 0x4b400000
	v_fmaak_f32 v51, v20, v48, 0x4b400000
	v_fmaak_f32 v52, v21, v48, 0x4b400000
	v_perm_b32 v49, v50, v49, s33
	v_perm_b32 v51, v52, v51, s34
	v_or_b32_e32 v72, v49, v51
	v_fmaak_f32 v41, v22, v48, 0x4b400000
	v_fmaak_f32 v42, v23, v48, 0x4b400000
	v_fmaak_f32 v43, v24, v48, 0x4b400000
	v_fmaak_f32 v44, v25, v48, 0x4b400000
	v_perm_b32 v41, v42, v41, s33
	v_perm_b32 v43, v44, v43, s34
	v_or_b32_e32 v73, v41, v43
	v_fmaak_f32 v49, v26, v48, 0x4b400000
	v_fmaak_f32 v50, v27, v48, 0x4b400000
	v_fmaak_f32 v51, v28, v48, 0x4b400000
	v_fmaak_f32 v52, v29, v48, 0x4b400000
	v_perm_b32 v49, v50, v49, s33
	v_perm_b32 v51, v52, v51, s34
	v_or_b32_e32 v74, v49, v51
	v_fmaak_f32 v41, v30, v48, 0x4b400000
	v_fmaak_f32 v42, v31, v48, 0x4b400000
	v_fmaak_f32 v43, v32, v48, 0x4b400000
	v_fmaak_f32 v44, v33, v48, 0x4b400000
	v_perm_b32 v41, v42, v41, s33
	v_perm_b32 v43, v44, v43, s34
	v_or_b32_e32 v75, v41, v43
	s_waitcnt vmcnt(0)
	ds_read_b128 v[18:21], v38 offset:0
	ds_read_b128 v[22:25], v38 offset:1024
	ds_read_b128 v[26:29], v38 offset:2048
	ds_read_b128 v[30:33], v38 offset:3072
	s_waitcnt lgkmcnt(0)
	s_barrier
	s_mov_b32 m0, s35
	s_nop 0
	global_load_lds_dwordx4 v34, s[16:17] nt
	global_load_lds_dwordx4 v34, s[16:17] offset:1024 nt
	global_load_lds_dwordx4 v34, s[16:17] offset:2048 nt
	global_load_lds_dwordx4 v35, s[16:17] offset:3072 nt
	s_add_u32 s16, s16, 0x7d00
	s_addc_u32 s17, s17, 0
	v_cndmask_b32_e64 v30, 0, v30, s[18:19]
	v_cndmask_b32_e64 v31, 0, v31, s[18:19]
	v_cndmask_b32_e64 v32, 0, v32, s[18:19]
	v_cndmask_b32_e64 v33, 0, v33, s[18:19]
	v_max3_f32 v41, |v18|, |v19|, |v20|
	v_max3_f32 v42, |v21|, |v22|, |v23|
	v_max3_f32 v43, |v24|, |v25|, |v26|
	v_max3_f32 v44, |v27|, |v28|, |v29|
	v_max3_f32 v48, |v30|, |v31|, |v32|
	v_max3_f32 v41, v41, v42, |v33|
	v_max3_f32 v43, v43, v44, v48
	v_max_f32_e32 v41, v41, v43
	v_pk_add_f32 v[2:3], v[2:3], v[18:19]
	v_pk_add_f32 v[4:5], v[4:5], v[20:21]
	v_max_f32_dpp v41, v41, v41 quad_perm:[1,0,3,2] row_mask:0xf bank_mask:0xf
	v_pk_add_f32 v[6:7], v[6:7], v[22:23]
	v_pk_add_f32 v[8:9], v[8:9], v[24:25]
	v_max_f32_dpp v41, v41, v41 quad_perm:[2,3,0,1] row_mask:0xf bank_mask:0xf
	v_pk_add_f32 v[10:11], v[10:11], v[26:27]
	v_pk_add_f32 v[12:13], v[12:13], v[28:29]
	v_max_f32_dpp v41, v41, v41 row_half_mirror row_mask:0xf bank_mask:0xf
	v_pk_add_f32 v[14:15], v[14:15], v[30:31]
	v_pk_add_f32 v[16:17], v[16:17], v[32:33]
	v_max_f32_dpp v41, v41, v41 row_mirror row_mask:0xf bank_mask:0xf
	s_nop 1
	v_max_f32_dpp v41, v41, v41 row_bcast:15 row_mask:0xa bank_mask:0xf
	s_nop 1
	v_max_f32_dpp v41, v41, v41 row_bcast:31 row_mask:0xc bank_mask:0xf
	s_nop 1
	v_readlane_b32 s28, v41, 63
	s_nop 1
	v_div_scale_f32 v48, s[30:31], s28, s28, v47
	v_rcp_f32_e32 v49, v48
	s_nop 0
	v_fma_f32 v50, -v48, v49, 1.0
	v_fmac_f32_e32 v49, v50, v49
	v_mov_b32_e32 v50, s28
	v_div_scale_f32 v50, vcc, s32, v50, s32
	v_mul_f32_e32 v51, v50, v49
	v_fma_f32 v52, -v48, v51, v50
	v_fmac_f32_e32 v51, v52, v49
	v_fma_f32 v48, -v48, v51, v50
	v_div_fmas_f32 v48, v48, v49, v51
	v_div_fixup_f32 v48, v48, s28, v47
	v_cmp_gt_f32_e64 vcc, s28, 0
	v_writelane_b32 v40, s28, 5
	s_nop 0
	v_cndmask_b32_e32 v48, 0, v48, vcc
	v_fmaak_f32 v49, v18, v48, 0x4b400000
	v_fmaak_f32 v50, v19, v48, 0x4b400000
	v_fmaak_f32 v51, v20, v48, 0x4b400000
	v_fmaak_f32 v52, v21, v48, 0x4b400000
	v_perm_b32 v49, v50, v49, s33
	v_perm_b32 v51, v52, v51, s34
	v_or_b32_e32 v76, v49, v51
	v_fmaak_f32 v41, v22, v48, 0x4b400000
	v_fmaak_f32 v42, v23, v48, 0x4b400000
	v_fmaak_f32 v43, v24, v48, 0x4b400000
	v_fmaak_f32 v44, v25, v48, 0x4b400000
	v_perm_b32 v41, v42, v41, s33
	v_perm_b32 v43, v44, v43, s34
	v_or_b32_e32 v77, v41, v43
	v_fmaak_f32 v49, v26, v48, 0x4b400000
	v_fmaak_f32 v50, v27, v48, 0x4b400000
	v_fmaak_f32 v51, v28, v48, 0x4b400000
	v_fmaak_f32 v52, v29, v48, 0x4b400000
	v_perm_b32 v49, v50, v49, s33
	v_perm_b32 v51, v52, v51, s34
	v_or_b32_e32 v78, v49, v51
	v_fmaak_f32 v41, v30, v48, 0x4b400000
	v_fmaak_f32 v42, v31, v48, 0x4b400000
	v_fmaak_f32 v43, v32, v48, 0x4b400000
	v_fmaak_f32 v44, v33, v48, 0x4b400000
	v_perm_b32 v41, v42, v41, s33
	v_perm_b32 v43, v44, v43, s34
	v_or_b32_e32 v79, v41, v43
	s_waitcnt vmcnt(0)
	ds_read_b128 v[18:21], v38 offset:0
	ds_read_b128 v[22:25], v38 offset:1024
	ds_read_b128 v[26:29], v38 offset:2048
	ds_read_b128 v[30:33], v38 offset:3072
	s_waitcnt lgkmcnt(0)
	s_barrier
	s_mov_b32 m0, s35
	s_nop 0
	global_load_lds_dwordx4 v34, s[16:17] nt
	global_load_lds_dwordx4 v34, s[16:17] offset:1024 nt
	global_load_lds_dwordx4 v34, s[16:17] offset:2048 nt
	global_load_lds_dwordx4 v35, s[16:17] offset:3072 nt
	s_add_u32 s16, s16, 0x7d00
	s_addc_u32 s17, s17, 0
	v_cndmask_b32_e64 v30, 0, v30, s[18:19]
	v_cndmask_b32_e64 v31, 0, v31, s[18:19]
	v_cndmask_b32_e64 v32, 0, v32, s[18:19]
	v_cndmask_b32_e64 v33, 0, v33, s[18:19]
	v_max3_f32 v41, |v18|, |v19|, |v20|
	v_max3_f32 v42, |v21|, |v22|, |v23|
	v_max3_f32 v43, |v24|, |v25|, |v26|
	v_max3_f32 v44, |v27|, |v28|, |v29|
	v_max3_f32 v48, |v30|, |v31|, |v32|
	v_max3_f32 v41, v41, v42, |v33|
	v_max3_f32 v43, v43, v44, v48
	v_max_f32_e32 v41, v41, v43
	v_pk_add_f32 v[2:3], v[2:3], v[18:19]
	v_pk_add_f32 v[4:5], v[4:5], v[20:21]
	v_max_f32_dpp v41, v41, v41 quad_perm:[1,0,3,2] row_mask:0xf bank_mask:0xf
	v_pk_add_f32 v[6:7], v[6:7], v[22:23]
	v_pk_add_f32 v[8:9], v[8:9], v[24:25]
	v_max_f32_dpp v41, v41, v41 quad_perm:[2,3,0,1] row_mask:0xf bank_mask:0xf
	v_pk_add_f32 v[10:11], v[10:11], v[26:27]
	v_pk_add_f32 v[12:13], v[12:13], v[28:29]
	v_max_f32_dpp v41, v41, v41 row_half_mirror row_mask:0xf bank_mask:0xf
	v_pk_add_f32 v[14:15], v[14:15], v[30:31]
	v_pk_add_f32 v[16:17], v[16:17], v[32:33]
	v_max_f32_dpp v41, v41, v41 row_mirror row_mask:0xf bank_mask:0xf
	s_nop 1
	v_max_f32_dpp v41, v41, v41 row_bcast:15 row_mask:0xa bank_mask:0xf
	s_nop 1
	v_max_f32_dpp v41, v41, v41 row_bcast:31 row_mask:0xc bank_mask:0xf
	s_nop 1
	v_readlane_b32 s28, v41, 63
	s_nop 1
	v_div_scale_f32 v48, s[30:31], s28, s28, v47
	v_rcp_f32_e32 v49, v48
	s_nop 0
	v_fma_f32 v50, -v48, v49, 1.0
	v_fmac_f32_e32 v49, v50, v49
	v_mov_b32_e32 v50, s28
	v_div_scale_f32 v50, vcc, s32, v50, s32
	v_mul_f32_e32 v51, v50, v49
	v_fma_f32 v52, -v48, v51, v50
	v_fmac_f32_e32 v51, v52, v49
	v_fma_f32 v48, -v48, v51, v50
	v_div_fmas_f32 v48, v48, v49, v51
	v_div_fixup_f32 v48, v48, s28, v47
	v_cmp_gt_f32_e64 vcc, s28, 0
	v_writelane_b32 v40, s28, 6
	s_nop 0
	v_cndmask_b32_e32 v48, 0, v48, vcc
	v_fmaak_f32 v49, v18, v48, 0x4b400000
	v_fmaak_f32 v50, v19, v48, 0x4b400000
	v_fmaak_f32 v51, v20, v48, 0x4b400000
	v_fmaak_f32 v52, v21, v48, 0x4b400000
	v_perm_b32 v49, v50, v49, s33
	v_perm_b32 v51, v52, v51, s34
	v_or_b32_e32 v80, v49, v51
	v_fmaak_f32 v41, v22, v48, 0x4b400000
	v_fmaak_f32 v42, v23, v48, 0x4b400000
	v_fmaak_f32 v43, v24, v48, 0x4b400000
	v_fmaak_f32 v44, v25, v48, 0x4b400000
	v_perm_b32 v41, v42, v41, s33
	v_perm_b32 v43, v44, v43, s34
	v_or_b32_e32 v81, v41, v43
	v_fmaak_f32 v49, v26, v48, 0x4b400000
	v_fmaak_f32 v50, v27, v48, 0x4b400000
	v_fmaak_f32 v51, v28, v48, 0x4b400000
	v_fmaak_f32 v52, v29, v48, 0x4b400000
	v_perm_b32 v49, v50, v49, s33
	v_perm_b32 v51, v52, v51, s34
	v_or_b32_e32 v82, v49, v51
	v_fmaak_f32 v41, v30, v48, 0x4b400000
	v_fmaak_f32 v42, v31, v48, 0x4b400000
	v_fmaak_f32 v43, v32, v48, 0x4b400000
	v_fmaak_f32 v44, v33, v48, 0x4b400000
	v_perm_b32 v41, v42, v41, s33
	v_perm_b32 v43, v44, v43, s34
	v_or_b32_e32 v83, v41, v43
	s_waitcnt vmcnt(0)
	ds_read_b128 v[18:21], v38 offset:0
	ds_read_b128 v[22:25], v38 offset:1024
	ds_read_b128 v[26:29], v38 offset:2048
	ds_read_b128 v[30:33], v38 offset:3072
	s_waitcnt lgkmcnt(0)
	s_barrier
	s_mov_b32 m0, s35
	s_nop 0
	global_load_lds_dwordx4 v34, s[16:17] nt
	global_load_lds_dwordx4 v34, s[16:17] offset:1024 nt
	global_load_lds_dwordx4 v34, s[16:17] offset:2048 nt
	global_load_lds_dwordx4 v35, s[16:17] offset:3072 nt
	s_add_u32 s16, s16, 0x7d00
	s_addc_u32 s17, s17, 0
	v_cndmask_b32_e64 v30, 0, v30, s[18:19]
	v_cndmask_b32_e64 v31, 0, v31, s[18:19]
	v_cndmask_b32_e64 v32, 0, v32, s[18:19]
	v_cndmask_b32_e64 v33, 0, v33, s[18:19]
	v_max3_f32 v41, |v18|, |v19|, |v20|
	v_max3_f32 v42, |v21|, |v22|, |v23|
	v_max3_f32 v43, |v24|, |v25|, |v26|
	v_max3_f32 v44, |v27|, |v28|, |v29|
	v_max3_f32 v48, |v30|, |v31|, |v32|
	v_max3_f32 v41, v41, v42, |v33|
	v_max3_f32 v43, v43, v44, v48
	v_max_f32_e32 v41, v41, v43
	v_pk_add_f32 v[2:3], v[2:3], v[18:19]
	v_pk_add_f32 v[4:5], v[4:5], v[20:21]
	v_max_f32_dpp v41, v41, v41 quad_perm:[1,0,3,2] row_mask:0xf bank_mask:0xf
	v_pk_add_f32 v[6:7], v[6:7], v[22:23]
	v_pk_add_f32 v[8:9], v[8:9], v[24:25]
	v_max_f32_dpp v41, v41, v41 quad_perm:[2,3,0,1] row_mask:0xf bank_mask:0xf
	v_pk_add_f32 v[10:11], v[10:11], v[26:27]
	v_pk_add_f32 v[12:13], v[12:13], v[28:29]
	v_max_f32_dpp v41, v41, v41 row_half_mirror row_mask:0xf bank_mask:0xf
	v_pk_add_f32 v[14:15], v[14:15], v[30:31]
	v_pk_add_f32 v[16:17], v[16:17], v[32:33]
	v_max_f32_dpp v41, v41, v41 row_mirror row_mask:0xf bank_mask:0xf
	s_nop 1
	v_max_f32_dpp v41, v41, v41 row_bcast:15 row_mask:0xa bank_mask:0xf
	s_nop 1
	v_max_f32_dpp v41, v41, v41 row_bcast:31 row_mask:0xc bank_mask:0xf
	s_nop 1
	v_readlane_b32 s28, v41, 63
	s_nop 1
	v_div_scale_f32 v48, s[30:31], s28, s28, v47
	v_rcp_f32_e32 v49, v48
	s_nop 0
	v_fma_f32 v50, -v48, v49, 1.0
	v_fmac_f32_e32 v49, v50, v49
	v_mov_b32_e32 v50, s28
	v_div_scale_f32 v50, vcc, s32, v50, s32
	v_mul_f32_e32 v51, v50, v49
	v_fma_f32 v52, -v48, v51, v50
	v_fmac_f32_e32 v51, v52, v49
	v_fma_f32 v48, -v48, v51, v50
	v_div_fmas_f32 v48, v48, v49, v51
	v_div_fixup_f32 v48, v48, s28, v47
	v_cmp_gt_f32_e64 vcc, s28, 0
	v_writelane_b32 v40, s28, 7
	s_nop 0
	v_cndmask_b32_e32 v48, 0, v48, vcc
	v_fmaak_f32 v49, v18, v48, 0x4b400000
	v_fmaak_f32 v50, v19, v48, 0x4b400000
	v_fmaak_f32 v51, v20, v48, 0x4b400000
	v_fmaak_f32 v52, v21, v48, 0x4b400000
	v_perm_b32 v49, v50, v49, s33
	v_perm_b32 v51, v52, v51, s34
	v_or_b32_e32 v84, v49, v51
	v_fmaak_f32 v41, v22, v48, 0x4b400000
	v_fmaak_f32 v42, v23, v48, 0x4b400000
	v_fmaak_f32 v43, v24, v48, 0x4b400000
	v_fmaak_f32 v44, v25, v48, 0x4b400000
	v_perm_b32 v41, v42, v41, s33
	v_perm_b32 v43, v44, v43, s34
	v_or_b32_e32 v85, v41, v43
	v_fmaak_f32 v49, v26, v48, 0x4b400000
	v_fmaak_f32 v50, v27, v48, 0x4b400000
	v_fmaak_f32 v51, v28, v48, 0x4b400000
	v_fmaak_f32 v52, v29, v48, 0x4b400000
	v_perm_b32 v49, v50, v49, s33
	v_perm_b32 v51, v52, v51, s34
	v_or_b32_e32 v86, v49, v51
	v_fmaak_f32 v41, v30, v48, 0x4b400000
	v_fmaak_f32 v42, v31, v48, 0x4b400000
	v_fmaak_f32 v43, v32, v48, 0x4b400000
	v_fmaak_f32 v44, v33, v48, 0x4b400000
	v_perm_b32 v41, v42, v41, s33
	v_perm_b32 v43, v44, v43, s34
	v_or_b32_e32 v87, v41, v43
	s_waitcnt vmcnt(0)
	ds_read_b128 v[18:21], v38 offset:0
	ds_read_b128 v[22:25], v38 offset:1024
	ds_read_b128 v[26:29], v38 offset:2048
	ds_read_b128 v[30:33], v38 offset:3072
	s_waitcnt lgkmcnt(0)
	s_barrier
	s_mov_b32 m0, s35
	s_nop 0
	global_load_lds_dwordx4 v34, s[16:17] nt
	global_load_lds_dwordx4 v34, s[16:17] offset:1024 nt
	global_load_lds_dwordx4 v34, s[16:17] offset:2048 nt
	global_load_lds_dwordx4 v35, s[16:17] offset:3072 nt
	s_add_u32 s16, s16, 0x7d00
	s_addc_u32 s17, s17, 0
	v_cndmask_b32_e64 v30, 0, v30, s[18:19]
	v_cndmask_b32_e64 v31, 0, v31, s[18:19]
	v_cndmask_b32_e64 v32, 0, v32, s[18:19]
	v_cndmask_b32_e64 v33, 0, v33, s[18:19]
	v_max3_f32 v41, |v18|, |v19|, |v20|
	v_max3_f32 v42, |v21|, |v22|, |v23|
	v_max3_f32 v43, |v24|, |v25|, |v26|
	v_max3_f32 v44, |v27|, |v28|, |v29|
	v_max3_f32 v48, |v30|, |v31|, |v32|
	v_max3_f32 v41, v41, v42, |v33|
	v_max3_f32 v43, v43, v44, v48
	v_max_f32_e32 v41, v41, v43
	v_pk_add_f32 v[2:3], v[2:3], v[18:19]
	v_pk_add_f32 v[4:5], v[4:5], v[20:21]
	v_max_f32_dpp v41, v41, v41 quad_perm:[1,0,3,2] row_mask:0xf bank_mask:0xf
	v_pk_add_f32 v[6:7], v[6:7], v[22:23]
	v_pk_add_f32 v[8:9], v[8:9], v[24:25]
	v_max_f32_dpp v41, v41, v41 quad_perm:[2,3,0,1] row_mask:0xf bank_mask:0xf
	v_pk_add_f32 v[10:11], v[10:11], v[26:27]
	v_pk_add_f32 v[12:13], v[12:13], v[28:29]
	v_max_f32_dpp v41, v41, v41 row_half_mirror row_mask:0xf bank_mask:0xf
	v_pk_add_f32 v[14:15], v[14:15], v[30:31]
	v_pk_add_f32 v[16:17], v[16:17], v[32:33]
	v_max_f32_dpp v41, v41, v41 row_mirror row_mask:0xf bank_mask:0xf
	s_nop 1
	v_max_f32_dpp v41, v41, v41 row_bcast:15 row_mask:0xa bank_mask:0xf
	s_nop 1
	v_max_f32_dpp v41, v41, v41 row_bcast:31 row_mask:0xc bank_mask:0xf
	s_nop 1
	v_readlane_b32 s28, v41, 63
	s_nop 1
	v_div_scale_f32 v48, s[30:31], s28, s28, v47
	v_rcp_f32_e32 v49, v48
	s_nop 0
	v_fma_f32 v50, -v48, v49, 1.0
	v_fmac_f32_e32 v49, v50, v49
	v_mov_b32_e32 v50, s28
	v_div_scale_f32 v50, vcc, s32, v50, s32
	v_mul_f32_e32 v51, v50, v49
	v_fma_f32 v52, -v48, v51, v50
	v_fmac_f32_e32 v51, v52, v49
	v_fma_f32 v48, -v48, v51, v50
	v_div_fmas_f32 v48, v48, v49, v51
	v_div_fixup_f32 v48, v48, s28, v47
	v_cmp_gt_f32_e64 vcc, s28, 0
	v_writelane_b32 v40, s28, 8
	s_nop 0
	v_cndmask_b32_e32 v48, 0, v48, vcc
	v_fmaak_f32 v49, v18, v48, 0x4b400000
	v_fmaak_f32 v50, v19, v48, 0x4b400000
	v_fmaak_f32 v51, v20, v48, 0x4b400000
	v_fmaak_f32 v52, v21, v48, 0x4b400000
	v_perm_b32 v49, v50, v49, s33
	v_perm_b32 v51, v52, v51, s34
	v_or_b32_e32 v88, v49, v51
	v_fmaak_f32 v41, v22, v48, 0x4b400000
	v_fmaak_f32 v42, v23, v48, 0x4b400000
	v_fmaak_f32 v43, v24, v48, 0x4b400000
	v_fmaak_f32 v44, v25, v48, 0x4b400000
	v_perm_b32 v41, v42, v41, s33
	v_perm_b32 v43, v44, v43, s34
	v_or_b32_e32 v89, v41, v43
	v_fmaak_f32 v49, v26, v48, 0x4b400000
	v_fmaak_f32 v50, v27, v48, 0x4b400000
	v_fmaak_f32 v51, v28, v48, 0x4b400000
	v_fmaak_f32 v52, v29, v48, 0x4b400000
	v_perm_b32 v49, v50, v49, s33
	v_perm_b32 v51, v52, v51, s34
	v_or_b32_e32 v90, v49, v51
	v_fmaak_f32 v41, v30, v48, 0x4b400000
	v_fmaak_f32 v42, v31, v48, 0x4b400000
	v_fmaak_f32 v43, v32, v48, 0x4b400000
	v_fmaak_f32 v44, v33, v48, 0x4b400000
	v_perm_b32 v41, v42, v41, s33
	v_perm_b32 v43, v44, v43, s34
	v_or_b32_e32 v91, v41, v43
	s_waitcnt vmcnt(0)
	ds_read_b128 v[18:21], v38 offset:0
	ds_read_b128 v[22:25], v38 offset:1024
	ds_read_b128 v[26:29], v38 offset:2048
	ds_read_b128 v[30:33], v38 offset:3072
	s_waitcnt lgkmcnt(0)
	s_barrier
	s_mov_b32 m0, s35
	s_nop 0
	global_load_lds_dwordx4 v34, s[16:17] nt
	global_load_lds_dwordx4 v34, s[16:17] offset:1024 nt
	global_load_lds_dwordx4 v34, s[16:17] offset:2048 nt
	global_load_lds_dwordx4 v35, s[16:17] offset:3072 nt
	s_add_u32 s16, s16, 0x7d00
	s_addc_u32 s17, s17, 0
	v_cndmask_b32_e64 v30, 0, v30, s[18:19]
	v_cndmask_b32_e64 v31, 0, v31, s[18:19]
	v_cndmask_b32_e64 v32, 0, v32, s[18:19]
	v_cndmask_b32_e64 v33, 0, v33, s[18:19]
	v_max3_f32 v41, |v18|, |v19|, |v20|
	v_max3_f32 v42, |v21|, |v22|, |v23|
	v_max3_f32 v43, |v24|, |v25|, |v26|
	v_max3_f32 v44, |v27|, |v28|, |v29|
	v_max3_f32 v48, |v30|, |v31|, |v32|
	v_max3_f32 v41, v41, v42, |v33|
	v_max3_f32 v43, v43, v44, v48
	v_max_f32_e32 v41, v41, v43
	v_pk_add_f32 v[2:3], v[2:3], v[18:19]
	v_pk_add_f32 v[4:5], v[4:5], v[20:21]
	v_max_f32_dpp v41, v41, v41 quad_perm:[1,0,3,2] row_mask:0xf bank_mask:0xf
	v_pk_add_f32 v[6:7], v[6:7], v[22:23]
	v_pk_add_f32 v[8:9], v[8:9], v[24:25]
	v_max_f32_dpp v41, v41, v41 quad_perm:[2,3,0,1] row_mask:0xf bank_mask:0xf
	v_pk_add_f32 v[10:11], v[10:11], v[26:27]
	v_pk_add_f32 v[12:13], v[12:13], v[28:29]
	v_max_f32_dpp v41, v41, v41 row_half_mirror row_mask:0xf bank_mask:0xf
	v_pk_add_f32 v[14:15], v[14:15], v[30:31]
	v_pk_add_f32 v[16:17], v[16:17], v[32:33]
	v_max_f32_dpp v41, v41, v41 row_mirror row_mask:0xf bank_mask:0xf
	s_nop 1
	v_max_f32_dpp v41, v41, v41 row_bcast:15 row_mask:0xa bank_mask:0xf
	s_nop 1
	v_max_f32_dpp v41, v41, v41 row_bcast:31 row_mask:0xc bank_mask:0xf
	s_nop 1
	v_readlane_b32 s28, v41, 63
	s_nop 1
	v_div_scale_f32 v48, s[30:31], s28, s28, v47
	v_rcp_f32_e32 v49, v48
	s_nop 0
	v_fma_f32 v50, -v48, v49, 1.0
	v_fmac_f32_e32 v49, v50, v49
	v_mov_b32_e32 v50, s28
	v_div_scale_f32 v50, vcc, s32, v50, s32
	v_mul_f32_e32 v51, v50, v49
	v_fma_f32 v52, -v48, v51, v50
	v_fmac_f32_e32 v51, v52, v49
	v_fma_f32 v48, -v48, v51, v50
	v_div_fmas_f32 v48, v48, v49, v51
	v_div_fixup_f32 v48, v48, s28, v47
	v_cmp_gt_f32_e64 vcc, s28, 0
	v_writelane_b32 v40, s28, 9
	s_nop 0
	v_cndmask_b32_e32 v48, 0, v48, vcc
	v_fmaak_f32 v49, v18, v48, 0x4b400000
	v_fmaak_f32 v50, v19, v48, 0x4b400000
	v_fmaak_f32 v51, v20, v48, 0x4b400000
	v_fmaak_f32 v52, v21, v48, 0x4b400000
	v_perm_b32 v49, v50, v49, s33
	v_perm_b32 v51, v52, v51, s34
	v_or_b32_e32 v92, v49, v51
	v_fmaak_f32 v41, v22, v48, 0x4b400000
	v_fmaak_f32 v42, v23, v48, 0x4b400000
	v_fmaak_f32 v43, v24, v48, 0x4b400000
	v_fmaak_f32 v44, v25, v48, 0x4b400000
	v_perm_b32 v41, v42, v41, s33
	v_perm_b32 v43, v44, v43, s34
	v_or_b32_e32 v93, v41, v43
	v_fmaak_f32 v49, v26, v48, 0x4b400000
	v_fmaak_f32 v50, v27, v48, 0x4b400000
	v_fmaak_f32 v51, v28, v48, 0x4b400000
	v_fmaak_f32 v52, v29, v48, 0x4b400000
	v_perm_b32 v49, v50, v49, s33
	v_perm_b32 v51, v52, v51, s34
	v_or_b32_e32 v94, v49, v51
	v_fmaak_f32 v41, v30, v48, 0x4b400000
	v_fmaak_f32 v42, v31, v48, 0x4b400000
	v_fmaak_f32 v43, v32, v48, 0x4b400000
	v_fmaak_f32 v44, v33, v48, 0x4b400000
	v_perm_b32 v41, v42, v41, s33
	v_perm_b32 v43, v44, v43, s34
	v_or_b32_e32 v95, v41, v43
	s_waitcnt vmcnt(0)
	ds_read_b128 v[18:21], v38 offset:0
	ds_read_b128 v[22:25], v38 offset:1024
	ds_read_b128 v[26:29], v38 offset:2048
	ds_read_b128 v[30:33], v38 offset:3072
	s_waitcnt lgkmcnt(0)
	s_barrier
	s_mov_b32 m0, s35
	s_nop 0
	global_load_lds_dwordx4 v34, s[16:17] nt
	global_load_lds_dwordx4 v34, s[16:17] offset:1024 nt
	global_load_lds_dwordx4 v34, s[16:17] offset:2048 nt
	global_load_lds_dwordx4 v35, s[16:17] offset:3072 nt
	s_add_u32 s16, s16, 0x7d00
	s_addc_u32 s17, s17, 0
	v_cndmask_b32_e64 v30, 0, v30, s[18:19]
	v_cndmask_b32_e64 v31, 0, v31, s[18:19]
	v_cndmask_b32_e64 v32, 0, v32, s[18:19]
	v_cndmask_b32_e64 v33, 0, v33, s[18:19]
	v_max3_f32 v41, |v18|, |v19|, |v20|
	v_max3_f32 v42, |v21|, |v22|, |v23|
	v_max3_f32 v43, |v24|, |v25|, |v26|
	v_max3_f32 v44, |v27|, |v28|, |v29|
	v_max3_f32 v48, |v30|, |v31|, |v32|
	v_max3_f32 v41, v41, v42, |v33|
	v_max3_f32 v43, v43, v44, v48
	v_max_f32_e32 v41, v41, v43
	v_pk_add_f32 v[2:3], v[2:3], v[18:19]
	v_pk_add_f32 v[4:5], v[4:5], v[20:21]
	v_max_f32_dpp v41, v41, v41 quad_perm:[1,0,3,2] row_mask:0xf bank_mask:0xf
	v_pk_add_f32 v[6:7], v[6:7], v[22:23]
	v_pk_add_f32 v[8:9], v[8:9], v[24:25]
	v_max_f32_dpp v41, v41, v41 quad_perm:[2,3,0,1] row_mask:0xf bank_mask:0xf
	v_pk_add_f32 v[10:11], v[10:11], v[26:27]
	v_pk_add_f32 v[12:13], v[12:13], v[28:29]
	v_max_f32_dpp v41, v41, v41 row_half_mirror row_mask:0xf bank_mask:0xf
	v_pk_add_f32 v[14:15], v[14:15], v[30:31]
	v_pk_add_f32 v[16:17], v[16:17], v[32:33]
	v_max_f32_dpp v41, v41, v41 row_mirror row_mask:0xf bank_mask:0xf
	s_nop 1
	v_max_f32_dpp v41, v41, v41 row_bcast:15 row_mask:0xa bank_mask:0xf
	s_nop 1
	v_max_f32_dpp v41, v41, v41 row_bcast:31 row_mask:0xc bank_mask:0xf
	s_nop 1
	v_readlane_b32 s28, v41, 63
	s_nop 1
	v_div_scale_f32 v48, s[30:31], s28, s28, v47
	v_rcp_f32_e32 v49, v48
	s_nop 0
	v_fma_f32 v50, -v48, v49, 1.0
	v_fmac_f32_e32 v49, v50, v49
	v_mov_b32_e32 v50, s28
	v_div_scale_f32 v50, vcc, s32, v50, s32
	v_mul_f32_e32 v51, v50, v49
	v_fma_f32 v52, -v48, v51, v50
	v_fmac_f32_e32 v51, v52, v49
	v_fma_f32 v48, -v48, v51, v50
	v_div_fmas_f32 v48, v48, v49, v51
	v_div_fixup_f32 v48, v48, s28, v47
	v_cmp_gt_f32_e64 vcc, s28, 0
	v_writelane_b32 v40, s28, 10
	s_nop 0
	v_cndmask_b32_e32 v48, 0, v48, vcc
	v_fmaak_f32 v49, v18, v48, 0x4b400000
	v_fmaak_f32 v50, v19, v48, 0x4b400000
	v_fmaak_f32 v51, v20, v48, 0x4b400000
	v_fmaak_f32 v52, v21, v48, 0x4b400000
	v_perm_b32 v49, v50, v49, s33
	v_perm_b32 v51, v52, v51, s34
	v_or_b32_e32 v96, v49, v51
	v_fmaak_f32 v41, v22, v48, 0x4b400000
	v_fmaak_f32 v42, v23, v48, 0x4b400000
	v_fmaak_f32 v43, v24, v48, 0x4b400000
	v_fmaak_f32 v44, v25, v48, 0x4b400000
	v_perm_b32 v41, v42, v41, s33
	v_perm_b32 v43, v44, v43, s34
	v_or_b32_e32 v97, v41, v43
	v_fmaak_f32 v49, v26, v48, 0x4b400000
	v_fmaak_f32 v50, v27, v48, 0x4b400000
	v_fmaak_f32 v51, v28, v48, 0x4b400000
	v_fmaak_f32 v52, v29, v48, 0x4b400000
	v_perm_b32 v49, v50, v49, s33
	v_perm_b32 v51, v52, v51, s34
	v_or_b32_e32 v98, v49, v51
	v_fmaak_f32 v41, v30, v48, 0x4b400000
	v_fmaak_f32 v42, v31, v48, 0x4b400000
	v_fmaak_f32 v43, v32, v48, 0x4b400000
	v_fmaak_f32 v44, v33, v48, 0x4b400000
	v_perm_b32 v41, v42, v41, s33
	v_perm_b32 v43, v44, v43, s34
	v_or_b32_e32 v99, v41, v43
	s_waitcnt vmcnt(0)
	ds_read_b128 v[18:21], v38 offset:0
	ds_read_b128 v[22:25], v38 offset:1024
	ds_read_b128 v[26:29], v38 offset:2048
	ds_read_b128 v[30:33], v38 offset:3072
	s_waitcnt lgkmcnt(0)
	s_barrier
	s_mov_b32 m0, s35
	s_nop 0
	global_load_lds_dwordx4 v34, s[16:17] nt
	global_load_lds_dwordx4 v34, s[16:17] offset:1024 nt
	global_load_lds_dwordx4 v34, s[16:17] offset:2048 nt
	global_load_lds_dwordx4 v35, s[16:17] offset:3072 nt
	s_add_u32 s16, s16, 0x7d00
	s_addc_u32 s17, s17, 0
	v_cndmask_b32_e64 v30, 0, v30, s[18:19]
	v_cndmask_b32_e64 v31, 0, v31, s[18:19]
	v_cndmask_b32_e64 v32, 0, v32, s[18:19]
	v_cndmask_b32_e64 v33, 0, v33, s[18:19]
	v_max3_f32 v41, |v18|, |v19|, |v20|
	v_max3_f32 v42, |v21|, |v22|, |v23|
	v_max3_f32 v43, |v24|, |v25|, |v26|
	v_max3_f32 v44, |v27|, |v28|, |v29|
	v_max3_f32 v48, |v30|, |v31|, |v32|
	v_max3_f32 v41, v41, v42, |v33|
	v_max3_f32 v43, v43, v44, v48
	v_max_f32_e32 v41, v41, v43
	v_pk_add_f32 v[2:3], v[2:3], v[18:19]
	v_pk_add_f32 v[4:5], v[4:5], v[20:21]
	v_max_f32_dpp v41, v41, v41 quad_perm:[1,0,3,2] row_mask:0xf bank_mask:0xf
	v_pk_add_f32 v[6:7], v[6:7], v[22:23]
	v_pk_add_f32 v[8:9], v[8:9], v[24:25]
	v_max_f32_dpp v41, v41, v41 quad_perm:[2,3,0,1] row_mask:0xf bank_mask:0xf
	v_pk_add_f32 v[10:11], v[10:11], v[26:27]
	v_pk_add_f32 v[12:13], v[12:13], v[28:29]
	v_max_f32_dpp v41, v41, v41 row_half_mirror row_mask:0xf bank_mask:0xf
	v_pk_add_f32 v[14:15], v[14:15], v[30:31]
	v_pk_add_f32 v[16:17], v[16:17], v[32:33]
	v_max_f32_dpp v41, v41, v41 row_mirror row_mask:0xf bank_mask:0xf
	s_nop 1
	v_max_f32_dpp v41, v41, v41 row_bcast:15 row_mask:0xa bank_mask:0xf
	s_nop 1
	v_max_f32_dpp v41, v41, v41 row_bcast:31 row_mask:0xc bank_mask:0xf
	s_nop 1
	v_readlane_b32 s28, v41, 63
	s_nop 1
	v_div_scale_f32 v48, s[30:31], s28, s28, v47
	v_rcp_f32_e32 v49, v48
	s_nop 0
	v_fma_f32 v50, -v48, v49, 1.0
	v_fmac_f32_e32 v49, v50, v49
	v_mov_b32_e32 v50, s28
	v_div_scale_f32 v50, vcc, s32, v50, s32
	v_mul_f32_e32 v51, v50, v49
	v_fma_f32 v52, -v48, v51, v50
	v_fmac_f32_e32 v51, v52, v49
	v_fma_f32 v48, -v48, v51, v50
	v_div_fmas_f32 v48, v48, v49, v51
	v_div_fixup_f32 v48, v48, s28, v47
	v_cmp_gt_f32_e64 vcc, s28, 0
	v_writelane_b32 v40, s28, 11
	s_nop 0
	v_cndmask_b32_e32 v48, 0, v48, vcc
	v_fmaak_f32 v49, v18, v48, 0x4b400000
	v_fmaak_f32 v50, v19, v48, 0x4b400000
	v_fmaak_f32 v51, v20, v48, 0x4b400000
	v_fmaak_f32 v52, v21, v48, 0x4b400000
	v_perm_b32 v49, v50, v49, s33
	v_perm_b32 v51, v52, v51, s34
	v_or_b32_e32 v100, v49, v51
	v_fmaak_f32 v41, v22, v48, 0x4b400000
	v_fmaak_f32 v42, v23, v48, 0x4b400000
	v_fmaak_f32 v43, v24, v48, 0x4b400000
	v_fmaak_f32 v44, v25, v48, 0x4b400000
	v_perm_b32 v41, v42, v41, s33
	v_perm_b32 v43, v44, v43, s34
	v_or_b32_e32 v101, v41, v43
	v_fmaak_f32 v49, v26, v48, 0x4b400000
	v_fmaak_f32 v50, v27, v48, 0x4b400000
	v_fmaak_f32 v51, v28, v48, 0x4b400000
	v_fmaak_f32 v52, v29, v48, 0x4b400000
	v_perm_b32 v49, v50, v49, s33
	v_perm_b32 v51, v52, v51, s34
	v_or_b32_e32 v102, v49, v51
	v_fmaak_f32 v41, v30, v48, 0x4b400000
	v_fmaak_f32 v42, v31, v48, 0x4b400000
	v_fmaak_f32 v43, v32, v48, 0x4b400000
	v_fmaak_f32 v44, v33, v48, 0x4b400000
	v_perm_b32 v41, v42, v41, s33
	v_perm_b32 v43, v44, v43, s34
	v_or_b32_e32 v103, v41, v43
	s_waitcnt vmcnt(0)
	ds_read_b128 v[18:21], v38 offset:0
	ds_read_b128 v[22:25], v38 offset:1024
	ds_read_b128 v[26:29], v38 offset:2048
	ds_read_b128 v[30:33], v38 offset:3072
	s_waitcnt lgkmcnt(0)
	s_barrier
	s_mov_b32 m0, s35
	s_nop 0
	global_load_lds_dwordx4 v34, s[16:17] nt
	global_load_lds_dwordx4 v34, s[16:17] offset:1024 nt
	global_load_lds_dwordx4 v34, s[16:17] offset:2048 nt
	global_load_lds_dwordx4 v35, s[16:17] offset:3072 nt
	s_add_u32 s16, s16, 0x7d00
	s_addc_u32 s17, s17, 0
	v_cndmask_b32_e64 v30, 0, v30, s[18:19]
	v_cndmask_b32_e64 v31, 0, v31, s[18:19]
	v_cndmask_b32_e64 v32, 0, v32, s[18:19]
	v_cndmask_b32_e64 v33, 0, v33, s[18:19]
	v_max3_f32 v41, |v18|, |v19|, |v20|
	v_max3_f32 v42, |v21|, |v22|, |v23|
	v_max3_f32 v43, |v24|, |v25|, |v26|
	v_max3_f32 v44, |v27|, |v28|, |v29|
	v_max3_f32 v48, |v30|, |v31|, |v32|
	v_max3_f32 v41, v41, v42, |v33|
	v_max3_f32 v43, v43, v44, v48
	v_max_f32_e32 v41, v41, v43
	v_pk_add_f32 v[2:3], v[2:3], v[18:19]
	v_pk_add_f32 v[4:5], v[4:5], v[20:21]
	v_max_f32_dpp v41, v41, v41 quad_perm:[1,0,3,2] row_mask:0xf bank_mask:0xf
	v_pk_add_f32 v[6:7], v[6:7], v[22:23]
	v_pk_add_f32 v[8:9], v[8:9], v[24:25]
	v_max_f32_dpp v41, v41, v41 quad_perm:[2,3,0,1] row_mask:0xf bank_mask:0xf
	v_pk_add_f32 v[10:11], v[10:11], v[26:27]
	v_pk_add_f32 v[12:13], v[12:13], v[28:29]
	v_max_f32_dpp v41, v41, v41 row_half_mirror row_mask:0xf bank_mask:0xf
	v_pk_add_f32 v[14:15], v[14:15], v[30:31]
	v_pk_add_f32 v[16:17], v[16:17], v[32:33]
	v_max_f32_dpp v41, v41, v41 row_mirror row_mask:0xf bank_mask:0xf
	s_nop 1
	v_max_f32_dpp v41, v41, v41 row_bcast:15 row_mask:0xa bank_mask:0xf
	s_nop 1
	v_max_f32_dpp v41, v41, v41 row_bcast:31 row_mask:0xc bank_mask:0xf
	s_nop 1
	v_readlane_b32 s28, v41, 63
	s_nop 1
	v_div_scale_f32 v48, s[30:31], s28, s28, v47
	v_rcp_f32_e32 v49, v48
	s_nop 0
	v_fma_f32 v50, -v48, v49, 1.0
	v_fmac_f32_e32 v49, v50, v49
	v_mov_b32_e32 v50, s28
	v_div_scale_f32 v50, vcc, s32, v50, s32
	v_mul_f32_e32 v51, v50, v49
	v_fma_f32 v52, -v48, v51, v50
	v_fmac_f32_e32 v51, v52, v49
	v_fma_f32 v48, -v48, v51, v50
	v_div_fmas_f32 v48, v48, v49, v51
	v_div_fixup_f32 v48, v48, s28, v47
	v_cmp_gt_f32_e64 vcc, s28, 0
	v_writelane_b32 v40, s28, 12
	s_nop 0
	v_cndmask_b32_e32 v48, 0, v48, vcc
	v_fmaak_f32 v49, v18, v48, 0x4b400000
	v_fmaak_f32 v50, v19, v48, 0x4b400000
	v_fmaak_f32 v51, v20, v48, 0x4b400000
	v_fmaak_f32 v52, v21, v48, 0x4b400000
	v_perm_b32 v49, v50, v49, s33
	v_perm_b32 v51, v52, v51, s34
	v_or_b32_e32 v104, v49, v51
	v_fmaak_f32 v41, v22, v48, 0x4b400000
	v_fmaak_f32 v42, v23, v48, 0x4b400000
	v_fmaak_f32 v43, v24, v48, 0x4b400000
	v_fmaak_f32 v44, v25, v48, 0x4b400000
	v_perm_b32 v41, v42, v41, s33
	v_perm_b32 v43, v44, v43, s34
	v_or_b32_e32 v105, v41, v43
	v_fmaak_f32 v49, v26, v48, 0x4b400000
	v_fmaak_f32 v50, v27, v48, 0x4b400000
	v_fmaak_f32 v51, v28, v48, 0x4b400000
	v_fmaak_f32 v52, v29, v48, 0x4b400000
	v_perm_b32 v49, v50, v49, s33
	v_perm_b32 v51, v52, v51, s34
	v_or_b32_e32 v106, v49, v51
	v_fmaak_f32 v41, v30, v48, 0x4b400000
	v_fmaak_f32 v42, v31, v48, 0x4b400000
	v_fmaak_f32 v43, v32, v48, 0x4b400000
	v_fmaak_f32 v44, v33, v48, 0x4b400000
	v_perm_b32 v41, v42, v41, s33
	v_perm_b32 v43, v44, v43, s34
	v_or_b32_e32 v107, v41, v43
	s_waitcnt vmcnt(0)
	ds_read_b128 v[18:21], v38 offset:0
	ds_read_b128 v[22:25], v38 offset:1024
	ds_read_b128 v[26:29], v38 offset:2048
	ds_read_b128 v[30:33], v38 offset:3072
	s_waitcnt lgkmcnt(0)
	s_barrier
	s_mov_b32 m0, s35
	s_nop 0
	global_load_lds_dwordx4 v34, s[16:17] nt
	global_load_lds_dwordx4 v34, s[16:17] offset:1024 nt
	global_load_lds_dwordx4 v34, s[16:17] offset:2048 nt
	global_load_lds_dwordx4 v35, s[16:17] offset:3072 nt
	s_add_u32 s16, s16, 0x7d00
	s_addc_u32 s17, s17, 0
	v_cndmask_b32_e64 v30, 0, v30, s[18:19]
	v_cndmask_b32_e64 v31, 0, v31, s[18:19]
	v_cndmask_b32_e64 v32, 0, v32, s[18:19]
	v_cndmask_b32_e64 v33, 0, v33, s[18:19]
	v_max3_f32 v41, |v18|, |v19|, |v20|
	v_max3_f32 v42, |v21|, |v22|, |v23|
	v_max3_f32 v43, |v24|, |v25|, |v26|
	v_max3_f32 v44, |v27|, |v28|, |v29|
	v_max3_f32 v48, |v30|, |v31|, |v32|
	v_max3_f32 v41, v41, v42, |v33|
	v_max3_f32 v43, v43, v44, v48
	v_max_f32_e32 v41, v41, v43
	v_pk_add_f32 v[2:3], v[2:3], v[18:19]
	v_pk_add_f32 v[4:5], v[4:5], v[20:21]
	v_max_f32_dpp v41, v41, v41 quad_perm:[1,0,3,2] row_mask:0xf bank_mask:0xf
	v_pk_add_f32 v[6:7], v[6:7], v[22:23]
	v_pk_add_f32 v[8:9], v[8:9], v[24:25]
	v_max_f32_dpp v41, v41, v41 quad_perm:[2,3,0,1] row_mask:0xf bank_mask:0xf
	v_pk_add_f32 v[10:11], v[10:11], v[26:27]
	v_pk_add_f32 v[12:13], v[12:13], v[28:29]
	v_max_f32_dpp v41, v41, v41 row_half_mirror row_mask:0xf bank_mask:0xf
	v_pk_add_f32 v[14:15], v[14:15], v[30:31]
	v_pk_add_f32 v[16:17], v[16:17], v[32:33]
	v_max_f32_dpp v41, v41, v41 row_mirror row_mask:0xf bank_mask:0xf
	s_nop 1
	v_max_f32_dpp v41, v41, v41 row_bcast:15 row_mask:0xa bank_mask:0xf
	s_nop 1
	v_max_f32_dpp v41, v41, v41 row_bcast:31 row_mask:0xc bank_mask:0xf
	s_nop 1
	v_readlane_b32 s28, v41, 63
	s_nop 1
	v_div_scale_f32 v48, s[30:31], s28, s28, v47
	v_rcp_f32_e32 v49, v48
	s_nop 0
	v_fma_f32 v50, -v48, v49, 1.0
	v_fmac_f32_e32 v49, v50, v49
	v_mov_b32_e32 v50, s28
	v_div_scale_f32 v50, vcc, s32, v50, s32
	v_mul_f32_e32 v51, v50, v49
	v_fma_f32 v52, -v48, v51, v50
	v_fmac_f32_e32 v51, v52, v49
	v_fma_f32 v48, -v48, v51, v50
	v_div_fmas_f32 v48, v48, v49, v51
	v_div_fixup_f32 v48, v48, s28, v47
	v_cmp_gt_f32_e64 vcc, s28, 0
	v_writelane_b32 v40, s28, 13
	s_nop 0
	v_cndmask_b32_e32 v48, 0, v48, vcc
	v_fmaak_f32 v49, v18, v48, 0x4b400000
	v_fmaak_f32 v50, v19, v48, 0x4b400000
	v_fmaak_f32 v51, v20, v48, 0x4b400000
	v_fmaak_f32 v52, v21, v48, 0x4b400000
	v_perm_b32 v49, v50, v49, s33
	v_perm_b32 v51, v52, v51, s34
	v_or_b32_e32 v108, v49, v51
	v_fmaak_f32 v41, v22, v48, 0x4b400000
	v_fmaak_f32 v42, v23, v48, 0x4b400000
	v_fmaak_f32 v43, v24, v48, 0x4b400000
	v_fmaak_f32 v44, v25, v48, 0x4b400000
	v_perm_b32 v41, v42, v41, s33
	v_perm_b32 v43, v44, v43, s34
	v_or_b32_e32 v109, v41, v43
	v_fmaak_f32 v49, v26, v48, 0x4b400000
	v_fmaak_f32 v50, v27, v48, 0x4b400000
	v_fmaak_f32 v51, v28, v48, 0x4b400000
	v_fmaak_f32 v52, v29, v48, 0x4b400000
	v_perm_b32 v49, v50, v49, s33
	v_perm_b32 v51, v52, v51, s34
	v_or_b32_e32 v110, v49, v51
	v_fmaak_f32 v41, v30, v48, 0x4b400000
	v_fmaak_f32 v42, v31, v48, 0x4b400000
	v_fmaak_f32 v43, v32, v48, 0x4b400000
	v_fmaak_f32 v44, v33, v48, 0x4b400000
	v_perm_b32 v41, v42, v41, s33
	v_perm_b32 v43, v44, v43, s34
	v_or_b32_e32 v111, v41, v43
	s_waitcnt vmcnt(0)
	ds_read_b128 v[18:21], v38 offset:0
	ds_read_b128 v[22:25], v38 offset:1024
	ds_read_b128 v[26:29], v38 offset:2048
	ds_read_b128 v[30:33], v38 offset:3072
	s_waitcnt lgkmcnt(0)
	s_barrier
	s_mov_b32 m0, s35
	s_nop 0
	global_load_lds_dwordx4 v34, s[16:17] nt
	global_load_lds_dwordx4 v34, s[16:17] offset:1024 nt
	global_load_lds_dwordx4 v34, s[16:17] offset:2048 nt
	global_load_lds_dwordx4 v35, s[16:17] offset:3072 nt
	s_add_u32 s16, s16, 0x7d00
	s_addc_u32 s17, s17, 0
	v_cndmask_b32_e64 v30, 0, v30, s[18:19]
	v_cndmask_b32_e64 v31, 0, v31, s[18:19]
	v_cndmask_b32_e64 v32, 0, v32, s[18:19]
	v_cndmask_b32_e64 v33, 0, v33, s[18:19]
	v_max3_f32 v41, |v18|, |v19|, |v20|
	v_max3_f32 v42, |v21|, |v22|, |v23|
	v_max3_f32 v43, |v24|, |v25|, |v26|
	v_max3_f32 v44, |v27|, |v28|, |v29|
	v_max3_f32 v48, |v30|, |v31|, |v32|
	v_max3_f32 v41, v41, v42, |v33|
	v_max3_f32 v43, v43, v44, v48
	v_max_f32_e32 v41, v41, v43
	v_pk_add_f32 v[2:3], v[2:3], v[18:19]
	v_pk_add_f32 v[4:5], v[4:5], v[20:21]
	v_max_f32_dpp v41, v41, v41 quad_perm:[1,0,3,2] row_mask:0xf bank_mask:0xf
	v_pk_add_f32 v[6:7], v[6:7], v[22:23]
	v_pk_add_f32 v[8:9], v[8:9], v[24:25]
	v_max_f32_dpp v41, v41, v41 quad_perm:[2,3,0,1] row_mask:0xf bank_mask:0xf
	v_pk_add_f32 v[10:11], v[10:11], v[26:27]
	v_pk_add_f32 v[12:13], v[12:13], v[28:29]
	v_max_f32_dpp v41, v41, v41 row_half_mirror row_mask:0xf bank_mask:0xf
	v_pk_add_f32 v[14:15], v[14:15], v[30:31]
	v_pk_add_f32 v[16:17], v[16:17], v[32:33]
	v_max_f32_dpp v41, v41, v41 row_mirror row_mask:0xf bank_mask:0xf
	s_nop 1
	v_max_f32_dpp v41, v41, v41 row_bcast:15 row_mask:0xa bank_mask:0xf
	s_nop 1
	v_max_f32_dpp v41, v41, v41 row_bcast:31 row_mask:0xc bank_mask:0xf
	s_nop 1
	v_readlane_b32 s28, v41, 63
	s_nop 1
	v_div_scale_f32 v48, s[30:31], s28, s28, v47
	v_rcp_f32_e32 v49, v48
	s_nop 0
	v_fma_f32 v50, -v48, v49, 1.0
	v_fmac_f32_e32 v49, v50, v49
	v_mov_b32_e32 v50, s28
	v_div_scale_f32 v50, vcc, s32, v50, s32
	v_mul_f32_e32 v51, v50, v49
	v_fma_f32 v52, -v48, v51, v50
	v_fmac_f32_e32 v51, v52, v49
	v_fma_f32 v48, -v48, v51, v50
	v_div_fmas_f32 v48, v48, v49, v51
	v_div_fixup_f32 v48, v48, s28, v47
	v_cmp_gt_f32_e64 vcc, s28, 0
	v_writelane_b32 v40, s28, 14
	s_nop 0
	v_cndmask_b32_e32 v48, 0, v48, vcc
	v_fmaak_f32 v49, v18, v48, 0x4b400000
	v_fmaak_f32 v50, v19, v48, 0x4b400000
	v_fmaak_f32 v51, v20, v48, 0x4b400000
	v_fmaak_f32 v52, v21, v48, 0x4b400000
	v_perm_b32 v49, v50, v49, s33
	v_perm_b32 v51, v52, v51, s34
	v_or_b32_e32 v112, v49, v51
	v_fmaak_f32 v41, v22, v48, 0x4b400000
	v_fmaak_f32 v42, v23, v48, 0x4b400000
	v_fmaak_f32 v43, v24, v48, 0x4b400000
	v_fmaak_f32 v44, v25, v48, 0x4b400000
	v_perm_b32 v41, v42, v41, s33
	v_perm_b32 v43, v44, v43, s34
	v_or_b32_e32 v113, v41, v43
	v_fmaak_f32 v49, v26, v48, 0x4b400000
	v_fmaak_f32 v50, v27, v48, 0x4b400000
	v_fmaak_f32 v51, v28, v48, 0x4b400000
	v_fmaak_f32 v52, v29, v48, 0x4b400000
	v_perm_b32 v49, v50, v49, s33
	v_perm_b32 v51, v52, v51, s34
	v_or_b32_e32 v114, v49, v51
	v_fmaak_f32 v41, v30, v48, 0x4b400000
	v_fmaak_f32 v42, v31, v48, 0x4b400000
	v_fmaak_f32 v43, v32, v48, 0x4b400000
	v_fmaak_f32 v44, v33, v48, 0x4b400000
	v_perm_b32 v41, v42, v41, s33
	v_perm_b32 v43, v44, v43, s34
	v_or_b32_e32 v115, v41, v43
	s_waitcnt vmcnt(0)
	ds_read_b128 v[18:21], v38 offset:0
	ds_read_b128 v[22:25], v38 offset:1024
	ds_read_b128 v[26:29], v38 offset:2048
	ds_read_b128 v[30:33], v38 offset:3072
	s_waitcnt lgkmcnt(0)
	s_barrier
	s_mov_b32 m0, s35
	s_nop 0
	global_load_lds_dwordx4 v34, s[16:17] nt
	global_load_lds_dwordx4 v34, s[16:17] offset:1024 nt
	global_load_lds_dwordx4 v34, s[16:17] offset:2048 nt
	global_load_lds_dwordx4 v35, s[16:17] offset:3072 nt
	s_add_u32 s16, s16, 0x7d00
	s_addc_u32 s17, s17, 0
	v_cndmask_b32_e64 v30, 0, v30, s[18:19]
	v_cndmask_b32_e64 v31, 0, v31, s[18:19]
	v_cndmask_b32_e64 v32, 0, v32, s[18:19]
	v_cndmask_b32_e64 v33, 0, v33, s[18:19]
	v_max3_f32 v41, |v18|, |v19|, |v20|
	v_max3_f32 v42, |v21|, |v22|, |v23|
	v_max3_f32 v43, |v24|, |v25|, |v26|
	v_max3_f32 v44, |v27|, |v28|, |v29|
	v_max3_f32 v48, |v30|, |v31|, |v32|
	v_max3_f32 v41, v41, v42, |v33|
	v_max3_f32 v43, v43, v44, v48
	v_max_f32_e32 v41, v41, v43
	v_pk_add_f32 v[2:3], v[2:3], v[18:19]
	v_pk_add_f32 v[4:5], v[4:5], v[20:21]
	v_max_f32_dpp v41, v41, v41 quad_perm:[1,0,3,2] row_mask:0xf bank_mask:0xf
	v_pk_add_f32 v[6:7], v[6:7], v[22:23]
	v_pk_add_f32 v[8:9], v[8:9], v[24:25]
	v_max_f32_dpp v41, v41, v41 quad_perm:[2,3,0,1] row_mask:0xf bank_mask:0xf
	v_pk_add_f32 v[10:11], v[10:11], v[26:27]
	v_pk_add_f32 v[12:13], v[12:13], v[28:29]
	v_max_f32_dpp v41, v41, v41 row_half_mirror row_mask:0xf bank_mask:0xf
	v_pk_add_f32 v[14:15], v[14:15], v[30:31]
	v_pk_add_f32 v[16:17], v[16:17], v[32:33]
	v_max_f32_dpp v41, v41, v41 row_mirror row_mask:0xf bank_mask:0xf
	s_nop 1
	v_max_f32_dpp v41, v41, v41 row_bcast:15 row_mask:0xa bank_mask:0xf
	s_nop 1
	v_max_f32_dpp v41, v41, v41 row_bcast:31 row_mask:0xc bank_mask:0xf
	s_nop 1
	v_readlane_b32 s28, v41, 63
	s_nop 1
	v_div_scale_f32 v48, s[30:31], s28, s28, v47
	v_rcp_f32_e32 v49, v48
	s_nop 0
	v_fma_f32 v50, -v48, v49, 1.0
	v_fmac_f32_e32 v49, v50, v49
	v_mov_b32_e32 v50, s28
	v_div_scale_f32 v50, vcc, s32, v50, s32
	v_mul_f32_e32 v51, v50, v49
	v_fma_f32 v52, -v48, v51, v50
	v_fmac_f32_e32 v51, v52, v49
	v_fma_f32 v48, -v48, v51, v50
	v_div_fmas_f32 v48, v48, v49, v51
	v_div_fixup_f32 v48, v48, s28, v47
	v_cmp_gt_f32_e64 vcc, s28, 0
	v_writelane_b32 v40, s28, 15
	s_nop 0
	v_cndmask_b32_e32 v48, 0, v48, vcc
	v_fmaak_f32 v49, v18, v48, 0x4b400000
	v_fmaak_f32 v50, v19, v48, 0x4b400000
	v_fmaak_f32 v51, v20, v48, 0x4b400000
	v_fmaak_f32 v52, v21, v48, 0x4b400000
	v_perm_b32 v49, v50, v49, s33
	v_perm_b32 v51, v52, v51, s34
	v_or_b32_e32 v116, v49, v51
	v_fmaak_f32 v41, v22, v48, 0x4b400000
	v_fmaak_f32 v42, v23, v48, 0x4b400000
	v_fmaak_f32 v43, v24, v48, 0x4b400000
	v_fmaak_f32 v44, v25, v48, 0x4b400000
	v_perm_b32 v41, v42, v41, s33
	v_perm_b32 v43, v44, v43, s34
	v_or_b32_e32 v117, v41, v43
	v_fmaak_f32 v49, v26, v48, 0x4b400000
	v_fmaak_f32 v50, v27, v48, 0x4b400000
	v_fmaak_f32 v51, v28, v48, 0x4b400000
	v_fmaak_f32 v52, v29, v48, 0x4b400000
	v_perm_b32 v49, v50, v49, s33
	v_perm_b32 v51, v52, v51, s34
	v_or_b32_e32 v118, v49, v51
	v_fmaak_f32 v41, v30, v48, 0x4b400000
	v_fmaak_f32 v42, v31, v48, 0x4b400000
	v_fmaak_f32 v43, v32, v48, 0x4b400000
	v_fmaak_f32 v44, v33, v48, 0x4b400000
	v_perm_b32 v41, v42, v41, s33
	v_perm_b32 v43, v44, v43, s34
	v_or_b32_e32 v119, v41, v43
	s_waitcnt vmcnt(0)
	ds_read_b128 v[18:21], v38 offset:0
	ds_read_b128 v[22:25], v38 offset:1024
	ds_read_b128 v[26:29], v38 offset:2048
	ds_read_b128 v[30:33], v38 offset:3072
	s_waitcnt lgkmcnt(0)
	s_barrier
	s_mov_b32 m0, s35
	s_nop 0
	global_load_lds_dwordx4 v34, s[16:17] nt
	global_load_lds_dwordx4 v34, s[16:17] offset:1024 nt
	global_load_lds_dwordx4 v34, s[16:17] offset:2048 nt
	global_load_lds_dwordx4 v35, s[16:17] offset:3072 nt
	s_add_u32 s16, s16, 0x7d00
	s_addc_u32 s17, s17, 0
	v_cndmask_b32_e64 v30, 0, v30, s[18:19]
	v_cndmask_b32_e64 v31, 0, v31, s[18:19]
	v_cndmask_b32_e64 v32, 0, v32, s[18:19]
	v_cndmask_b32_e64 v33, 0, v33, s[18:19]
	v_max3_f32 v41, |v18|, |v19|, |v20|
	v_max3_f32 v42, |v21|, |v22|, |v23|
	v_max3_f32 v43, |v24|, |v25|, |v26|
	v_max3_f32 v44, |v27|, |v28|, |v29|
	v_max3_f32 v48, |v30|, |v31|, |v32|
	v_max3_f32 v41, v41, v42, |v33|
	v_max3_f32 v43, v43, v44, v48
	v_max_f32_e32 v41, v41, v43
	v_pk_add_f32 v[2:3], v[2:3], v[18:19]
	v_pk_add_f32 v[4:5], v[4:5], v[20:21]
	v_max_f32_dpp v41, v41, v41 quad_perm:[1,0,3,2] row_mask:0xf bank_mask:0xf
	v_pk_add_f32 v[6:7], v[6:7], v[22:23]
	v_pk_add_f32 v[8:9], v[8:9], v[24:25]
	v_max_f32_dpp v41, v41, v41 quad_perm:[2,3,0,1] row_mask:0xf bank_mask:0xf
	v_pk_add_f32 v[10:11], v[10:11], v[26:27]
	v_pk_add_f32 v[12:13], v[12:13], v[28:29]
	v_max_f32_dpp v41, v41, v41 row_half_mirror row_mask:0xf bank_mask:0xf
	v_pk_add_f32 v[14:15], v[14:15], v[30:31]
	v_pk_add_f32 v[16:17], v[16:17], v[32:33]
	v_max_f32_dpp v41, v41, v41 row_mirror row_mask:0xf bank_mask:0xf
	s_nop 1
	v_max_f32_dpp v41, v41, v41 row_bcast:15 row_mask:0xa bank_mask:0xf
	s_nop 1
	v_max_f32_dpp v41, v41, v41 row_bcast:31 row_mask:0xc bank_mask:0xf
	s_nop 1
	v_readlane_b32 s28, v41, 63
	s_nop 1
	v_div_scale_f32 v48, s[30:31], s28, s28, v47
	v_rcp_f32_e32 v49, v48
	s_nop 0
	v_fma_f32 v50, -v48, v49, 1.0
	v_fmac_f32_e32 v49, v50, v49
	v_mov_b32_e32 v50, s28
	v_div_scale_f32 v50, vcc, s32, v50, s32
	v_mul_f32_e32 v51, v50, v49
	v_fma_f32 v52, -v48, v51, v50
	v_fmac_f32_e32 v51, v52, v49
	v_fma_f32 v48, -v48, v51, v50
	v_div_fmas_f32 v48, v48, v49, v51
	v_div_fixup_f32 v48, v48, s28, v47
	v_cmp_gt_f32_e64 vcc, s28, 0
	v_writelane_b32 v40, s28, 16
	s_nop 0
	v_cndmask_b32_e32 v48, 0, v48, vcc
	v_fmaak_f32 v49, v18, v48, 0x4b400000
	v_fmaak_f32 v50, v19, v48, 0x4b400000
	v_fmaak_f32 v51, v20, v48, 0x4b400000
	v_fmaak_f32 v52, v21, v48, 0x4b400000
	v_perm_b32 v49, v50, v49, s33
	v_perm_b32 v51, v52, v51, s34
	v_or_b32_e32 v120, v49, v51
	v_fmaak_f32 v41, v22, v48, 0x4b400000
	v_fmaak_f32 v42, v23, v48, 0x4b400000
	v_fmaak_f32 v43, v24, v48, 0x4b400000
	v_fmaak_f32 v44, v25, v48, 0x4b400000
	v_perm_b32 v41, v42, v41, s33
	v_perm_b32 v43, v44, v43, s34
	v_or_b32_e32 v121, v41, v43
	v_fmaak_f32 v49, v26, v48, 0x4b400000
	v_fmaak_f32 v50, v27, v48, 0x4b400000
	v_fmaak_f32 v51, v28, v48, 0x4b400000
	v_fmaak_f32 v52, v29, v48, 0x4b400000
	v_perm_b32 v49, v50, v49, s33
	v_perm_b32 v51, v52, v51, s34
	v_or_b32_e32 v122, v49, v51
	v_fmaak_f32 v41, v30, v48, 0x4b400000
	v_fmaak_f32 v42, v31, v48, 0x4b400000
	v_fmaak_f32 v43, v32, v48, 0x4b400000
	v_fmaak_f32 v44, v33, v48, 0x4b400000
	v_perm_b32 v41, v42, v41, s33
	v_perm_b32 v43, v44, v43, s34
	v_or_b32_e32 v123, v41, v43
	s_waitcnt vmcnt(0)
	ds_read_b128 v[18:21], v38 offset:0
	ds_read_b128 v[22:25], v38 offset:1024
	ds_read_b128 v[26:29], v38 offset:2048
	ds_read_b128 v[30:33], v38 offset:3072
	s_waitcnt lgkmcnt(0)
	s_barrier
	s_mov_b32 m0, s35
	s_nop 0
	global_load_lds_dwordx4 v34, s[16:17] nt
	global_load_lds_dwordx4 v34, s[16:17] offset:1024 nt
	global_load_lds_dwordx4 v34, s[16:17] offset:2048 nt
	global_load_lds_dwordx4 v35, s[16:17] offset:3072 nt
	s_add_u32 s16, s16, 0x7d00
	s_addc_u32 s17, s17, 0
	v_cndmask_b32_e64 v30, 0, v30, s[18:19]
	v_cndmask_b32_e64 v31, 0, v31, s[18:19]
	v_cndmask_b32_e64 v32, 0, v32, s[18:19]
	v_cndmask_b32_e64 v33, 0, v33, s[18:19]
	v_max3_f32 v41, |v18|, |v19|, |v20|
	v_max3_f32 v42, |v21|, |v22|, |v23|
	v_max3_f32 v43, |v24|, |v25|, |v26|
	v_max3_f32 v44, |v27|, |v28|, |v29|
	v_max3_f32 v48, |v30|, |v31|, |v32|
	v_max3_f32 v41, v41, v42, |v33|
	v_max3_f32 v43, v43, v44, v48
	v_max_f32_e32 v41, v41, v43
	v_pk_add_f32 v[2:3], v[2:3], v[18:19]
	v_pk_add_f32 v[4:5], v[4:5], v[20:21]
	v_max_f32_dpp v41, v41, v41 quad_perm:[1,0,3,2] row_mask:0xf bank_mask:0xf
	v_pk_add_f32 v[6:7], v[6:7], v[22:23]
	v_pk_add_f32 v[8:9], v[8:9], v[24:25]
	v_max_f32_dpp v41, v41, v41 quad_perm:[2,3,0,1] row_mask:0xf bank_mask:0xf
	v_pk_add_f32 v[10:11], v[10:11], v[26:27]
	v_pk_add_f32 v[12:13], v[12:13], v[28:29]
	v_max_f32_dpp v41, v41, v41 row_half_mirror row_mask:0xf bank_mask:0xf
	v_pk_add_f32 v[14:15], v[14:15], v[30:31]
	v_pk_add_f32 v[16:17], v[16:17], v[32:33]
	v_max_f32_dpp v41, v41, v41 row_mirror row_mask:0xf bank_mask:0xf
	s_nop 1
	v_max_f32_dpp v41, v41, v41 row_bcast:15 row_mask:0xa bank_mask:0xf
	s_nop 1
	v_max_f32_dpp v41, v41, v41 row_bcast:31 row_mask:0xc bank_mask:0xf
	s_nop 1
	v_readlane_b32 s28, v41, 63
	s_nop 1
	v_div_scale_f32 v48, s[30:31], s28, s28, v47
	v_rcp_f32_e32 v49, v48
	s_nop 0
	v_fma_f32 v50, -v48, v49, 1.0
	v_fmac_f32_e32 v49, v50, v49
	v_mov_b32_e32 v50, s28
	v_div_scale_f32 v50, vcc, s32, v50, s32
	v_mul_f32_e32 v51, v50, v49
	v_fma_f32 v52, -v48, v51, v50
	v_fmac_f32_e32 v51, v52, v49
	v_fma_f32 v48, -v48, v51, v50
	v_div_fmas_f32 v48, v48, v49, v51
	v_div_fixup_f32 v48, v48, s28, v47
	v_cmp_gt_f32_e64 vcc, s28, 0
	v_writelane_b32 v40, s28, 17
	s_nop 0
	v_cndmask_b32_e32 v48, 0, v48, vcc
	v_fmaak_f32 v49, v18, v48, 0x4b400000
	v_fmaak_f32 v50, v19, v48, 0x4b400000
	v_fmaak_f32 v51, v20, v48, 0x4b400000
	v_fmaak_f32 v52, v21, v48, 0x4b400000
	v_perm_b32 v49, v50, v49, s33
	v_perm_b32 v51, v52, v51, s34
	v_or_b32_e32 v124, v49, v51
	v_fmaak_f32 v41, v22, v48, 0x4b400000
	v_fmaak_f32 v42, v23, v48, 0x4b400000
	v_fmaak_f32 v43, v24, v48, 0x4b400000
	v_fmaak_f32 v44, v25, v48, 0x4b400000
	v_perm_b32 v41, v42, v41, s33
	v_perm_b32 v43, v44, v43, s34
	v_or_b32_e32 v125, v41, v43
	v_fmaak_f32 v49, v26, v48, 0x4b400000
	v_fmaak_f32 v50, v27, v48, 0x4b400000
	v_fmaak_f32 v51, v28, v48, 0x4b400000
	v_fmaak_f32 v52, v29, v48, 0x4b400000
	v_perm_b32 v49, v50, v49, s33
	v_perm_b32 v51, v52, v51, s34
	v_or_b32_e32 v126, v49, v51
	v_fmaak_f32 v41, v30, v48, 0x4b400000
	v_fmaak_f32 v42, v31, v48, 0x4b400000
	v_fmaak_f32 v43, v32, v48, 0x4b400000
	v_fmaak_f32 v44, v33, v48, 0x4b400000
	v_perm_b32 v41, v42, v41, s33
	v_perm_b32 v43, v44, v43, s34
	v_or_b32_e32 v127, v41, v43
	s_waitcnt vmcnt(0)
	ds_read_b128 v[18:21], v38 offset:0
	ds_read_b128 v[22:25], v38 offset:1024
	ds_read_b128 v[26:29], v38 offset:2048
	ds_read_b128 v[30:33], v38 offset:3072
	s_waitcnt lgkmcnt(0)
	s_barrier
	s_mov_b32 m0, s35
	s_nop 0
	global_load_lds_dwordx4 v34, s[16:17] nt
	global_load_lds_dwordx4 v34, s[16:17] offset:1024 nt
	global_load_lds_dwordx4 v34, s[16:17] offset:2048 nt
	global_load_lds_dwordx4 v35, s[16:17] offset:3072 nt
	s_add_u32 s16, s16, 0x7d00
	s_addc_u32 s17, s17, 0
	v_cndmask_b32_e64 v30, 0, v30, s[18:19]
	v_cndmask_b32_e64 v31, 0, v31, s[18:19]
	v_cndmask_b32_e64 v32, 0, v32, s[18:19]
	v_cndmask_b32_e64 v33, 0, v33, s[18:19]
	v_max3_f32 v41, |v18|, |v19|, |v20|
	v_max3_f32 v42, |v21|, |v22|, |v23|
	v_max3_f32 v43, |v24|, |v25|, |v26|
	v_max3_f32 v44, |v27|, |v28|, |v29|
	v_max3_f32 v48, |v30|, |v31|, |v32|
	v_max3_f32 v41, v41, v42, |v33|
	v_max3_f32 v43, v43, v44, v48
	v_max_f32_e32 v41, v41, v43
	v_pk_add_f32 v[2:3], v[2:3], v[18:19]
	v_pk_add_f32 v[4:5], v[4:5], v[20:21]
	v_max_f32_dpp v41, v41, v41 quad_perm:[1,0,3,2] row_mask:0xf bank_mask:0xf
	v_pk_add_f32 v[6:7], v[6:7], v[22:23]
	v_pk_add_f32 v[8:9], v[8:9], v[24:25]
	v_max_f32_dpp v41, v41, v41 quad_perm:[2,3,0,1] row_mask:0xf bank_mask:0xf
	v_pk_add_f32 v[10:11], v[10:11], v[26:27]
	v_pk_add_f32 v[12:13], v[12:13], v[28:29]
	v_max_f32_dpp v41, v41, v41 row_half_mirror row_mask:0xf bank_mask:0xf
	v_pk_add_f32 v[14:15], v[14:15], v[30:31]
	v_pk_add_f32 v[16:17], v[16:17], v[32:33]
	v_max_f32_dpp v41, v41, v41 row_mirror row_mask:0xf bank_mask:0xf
	s_nop 1
	v_max_f32_dpp v41, v41, v41 row_bcast:15 row_mask:0xa bank_mask:0xf
	s_nop 1
	v_max_f32_dpp v41, v41, v41 row_bcast:31 row_mask:0xc bank_mask:0xf
	s_nop 1
	v_readlane_b32 s28, v41, 63
	s_nop 1
	v_div_scale_f32 v48, s[30:31], s28, s28, v47
	v_rcp_f32_e32 v49, v48
	s_nop 0
	v_fma_f32 v50, -v48, v49, 1.0
	v_fmac_f32_e32 v49, v50, v49
	v_mov_b32_e32 v50, s28
	v_div_scale_f32 v50, vcc, s32, v50, s32
	v_mul_f32_e32 v51, v50, v49
	v_fma_f32 v52, -v48, v51, v50
	v_fmac_f32_e32 v51, v52, v49
	v_fma_f32 v48, -v48, v51, v50
	v_div_fmas_f32 v48, v48, v49, v51
	v_div_fixup_f32 v48, v48, s28, v47
	v_cmp_gt_f32_e64 vcc, s28, 0
	v_writelane_b32 v40, s28, 18
	s_nop 0
	v_cndmask_b32_e32 v48, 0, v48, vcc
	v_fmaak_f32 v49, v18, v48, 0x4b400000
	v_fmaak_f32 v50, v19, v48, 0x4b400000
	v_fmaak_f32 v51, v20, v48, 0x4b400000
	v_fmaak_f32 v52, v21, v48, 0x4b400000
	v_perm_b32 v49, v50, v49, s33
	v_perm_b32 v51, v52, v51, s34
	v_or_b32_e32 v36, v49, v51
	v_fmaak_f32 v41, v22, v48, 0x4b400000
	v_fmaak_f32 v42, v23, v48, 0x4b400000
	v_fmaak_f32 v43, v24, v48, 0x4b400000
	v_fmaak_f32 v44, v25, v48, 0x4b400000
	v_perm_b32 v41, v42, v41, s33
	v_perm_b32 v43, v44, v43, s34
	v_or_b32_e32 v37, v41, v43
	v_fmaak_f32 v49, v26, v48, 0x4b400000
	v_fmaak_f32 v50, v27, v48, 0x4b400000
	v_fmaak_f32 v51, v28, v48, 0x4b400000
	v_fmaak_f32 v52, v29, v48, 0x4b400000
	v_perm_b32 v49, v50, v49, s33
	v_perm_b32 v51, v52, v51, s34
	v_or_b32_e32 v45, v49, v51
	v_fmaak_f32 v41, v30, v48, 0x4b400000
	v_fmaak_f32 v42, v31, v48, 0x4b400000
	v_fmaak_f32 v43, v32, v48, 0x4b400000
	v_fmaak_f32 v44, v33, v48, 0x4b400000
	v_perm_b32 v41, v42, v41, s33
	v_perm_b32 v43, v44, v43, s34
	v_or_b32_e32 v46, v41, v43
	s_waitcnt vmcnt(0)
	ds_read_b128 v[18:21], v38 offset:0
	ds_read_b128 v[22:25], v38 offset:1024
	ds_read_b128 v[26:29], v38 offset:2048
	ds_read_b128 v[30:33], v38 offset:3072
	s_waitcnt lgkmcnt(0)
	s_barrier
	s_mov_b32 m0, s35
	s_nop 0
	global_load_lds_dwordx4 v34, s[16:17] nt
	global_load_lds_dwordx4 v34, s[16:17] offset:1024 nt
	global_load_lds_dwordx4 v34, s[16:17] offset:2048 nt
	global_load_lds_dwordx4 v35, s[16:17] offset:3072 nt
	s_add_u32 s16, s16, 0x7d00
	s_addc_u32 s17, s17, 0
	v_cndmask_b32_e64 v30, 0, v30, s[18:19]
	v_cndmask_b32_e64 v31, 0, v31, s[18:19]
	v_cndmask_b32_e64 v32, 0, v32, s[18:19]
	v_cndmask_b32_e64 v33, 0, v33, s[18:19]
	v_max3_f32 v41, |v18|, |v19|, |v20|
	v_max3_f32 v42, |v21|, |v22|, |v23|
	v_max3_f32 v43, |v24|, |v25|, |v26|
	v_max3_f32 v44, |v27|, |v28|, |v29|
	v_max3_f32 v48, |v30|, |v31|, |v32|
	v_max3_f32 v41, v41, v42, |v33|
	v_max3_f32 v43, v43, v44, v48
	v_max_f32_e32 v41, v41, v43
	v_pk_add_f32 v[2:3], v[2:3], v[18:19]
	v_pk_add_f32 v[4:5], v[4:5], v[20:21]
	v_max_f32_dpp v41, v41, v41 quad_perm:[1,0,3,2] row_mask:0xf bank_mask:0xf
	v_pk_add_f32 v[6:7], v[6:7], v[22:23]
	v_pk_add_f32 v[8:9], v[8:9], v[24:25]
	v_max_f32_dpp v41, v41, v41 quad_perm:[2,3,0,1] row_mask:0xf bank_mask:0xf
	v_pk_add_f32 v[10:11], v[10:11], v[26:27]
	v_pk_add_f32 v[12:13], v[12:13], v[28:29]
	v_max_f32_dpp v41, v41, v41 row_half_mirror row_mask:0xf bank_mask:0xf
	v_pk_add_f32 v[14:15], v[14:15], v[30:31]
	v_pk_add_f32 v[16:17], v[16:17], v[32:33]
	v_max_f32_dpp v41, v41, v41 row_mirror row_mask:0xf bank_mask:0xf
	s_nop 1
	v_max_f32_dpp v41, v41, v41 row_bcast:15 row_mask:0xa bank_mask:0xf
	s_nop 1
	v_max_f32_dpp v41, v41, v41 row_bcast:31 row_mask:0xc bank_mask:0xf
	s_nop 1
	v_readlane_b32 s28, v41, 63
	s_nop 1
	v_div_scale_f32 v48, s[30:31], s28, s28, v47
	v_rcp_f32_e32 v49, v48
	s_nop 0
	v_fma_f32 v50, -v48, v49, 1.0
	v_fmac_f32_e32 v49, v50, v49
	v_mov_b32_e32 v50, s28
	v_div_scale_f32 v50, vcc, s32, v50, s32
	v_mul_f32_e32 v51, v50, v49
	v_fma_f32 v52, -v48, v51, v50
	v_fmac_f32_e32 v51, v52, v49
	v_fma_f32 v48, -v48, v51, v50
	v_div_fmas_f32 v48, v48, v49, v51
	v_div_fixup_f32 v48, v48, s28, v47
	v_cmp_gt_f32_e64 vcc, s28, 0
	v_writelane_b32 v40, s28, 19
	s_nop 0
	v_cndmask_b32_e32 v48, 0, v48, vcc
	v_fmaak_f32 v49, v18, v48, 0x4b400000
	v_fmaak_f32 v50, v19, v48, 0x4b400000
	v_fmaak_f32 v51, v20, v48, 0x4b400000
	v_fmaak_f32 v52, v21, v48, 0x4b400000
	v_perm_b32 v49, v50, v49, s33
	v_perm_b32 v51, v52, v51, s34
	v_or_b32_e32 v53, v49, v51
	v_fmaak_f32 v41, v22, v48, 0x4b400000
	v_fmaak_f32 v42, v23, v48, 0x4b400000
	v_fmaak_f32 v43, v24, v48, 0x4b400000
	v_fmaak_f32 v44, v25, v48, 0x4b400000
	v_perm_b32 v41, v42, v41, s33
	v_perm_b32 v43, v44, v43, s34
	v_or_b32_e32 v54, v41, v43
	v_fmaak_f32 v49, v26, v48, 0x4b400000
	v_fmaak_f32 v50, v27, v48, 0x4b400000
	v_fmaak_f32 v51, v28, v48, 0x4b400000
	v_fmaak_f32 v52, v29, v48, 0x4b400000
	v_perm_b32 v49, v50, v49, s33
	v_perm_b32 v51, v52, v51, s34
	v_or_b32_e32 v55, v49, v51
	v_fmaak_f32 v41, v30, v48, 0x4b400000
	v_fmaak_f32 v42, v31, v48, 0x4b400000
	v_fmaak_f32 v43, v32, v48, 0x4b400000
	v_fmaak_f32 v44, v33, v48, 0x4b400000
	v_perm_b32 v41, v42, v41, s33
	v_perm_b32 v43, v44, v43, s34
	v_or_b32_e32 v1, v41, v43
	s_waitcnt vmcnt(0)
	ds_read_b128 v[18:21], v38 offset:0
	ds_read_b128 v[22:25], v38 offset:1024
	ds_read_b128 v[26:29], v38 offset:2048
	ds_read_b128 v[30:33], v38 offset:3072
	s_waitcnt lgkmcnt(0)
	s_barrier
	s_mov_b32 m0, s35
	s_nop 0
	global_load_lds_dwordx4 v34, s[16:17] nt
	global_load_lds_dwordx4 v34, s[16:17] offset:1024 nt
	global_load_lds_dwordx4 v34, s[16:17] offset:2048 nt
	global_load_lds_dwordx4 v35, s[16:17] offset:3072 nt
	s_add_u32 s16, s16, 0x7d00
	s_addc_u32 s17, s17, 0
	v_cndmask_b32_e64 v30, 0, v30, s[18:19]
	v_cndmask_b32_e64 v31, 0, v31, s[18:19]
	v_cndmask_b32_e64 v32, 0, v32, s[18:19]
	v_cndmask_b32_e64 v33, 0, v33, s[18:19]
	v_max3_f32 v41, |v18|, |v19|, |v20|
	v_max3_f32 v42, |v21|, |v22|, |v23|
	v_max3_f32 v43, |v24|, |v25|, |v26|
	v_max3_f32 v44, |v27|, |v28|, |v29|
	v_max3_f32 v48, |v30|, |v31|, |v32|
	v_max3_f32 v41, v41, v42, |v33|
	v_max3_f32 v43, v43, v44, v48
	v_max_f32_e32 v41, v41, v43
	v_pk_add_f32 v[2:3], v[2:3], v[18:19]
	v_pk_add_f32 v[4:5], v[4:5], v[20:21]
	v_max_f32_dpp v41, v41, v41 quad_perm:[1,0,3,2] row_mask:0xf bank_mask:0xf
	v_pk_add_f32 v[6:7], v[6:7], v[22:23]
	v_pk_add_f32 v[8:9], v[8:9], v[24:25]
	v_max_f32_dpp v41, v41, v41 quad_perm:[2,3,0,1] row_mask:0xf bank_mask:0xf
	v_pk_add_f32 v[10:11], v[10:11], v[26:27]
	v_pk_add_f32 v[12:13], v[12:13], v[28:29]
	v_max_f32_dpp v41, v41, v41 row_half_mirror row_mask:0xf bank_mask:0xf
	v_pk_add_f32 v[14:15], v[14:15], v[30:31]
	v_pk_add_f32 v[16:17], v[16:17], v[32:33]
	v_max_f32_dpp v41, v41, v41 row_mirror row_mask:0xf bank_mask:0xf
	s_nop 1
	v_max_f32_dpp v41, v41, v41 row_bcast:15 row_mask:0xa bank_mask:0xf
	s_nop 1
	v_max_f32_dpp v41, v41, v41 row_bcast:31 row_mask:0xc bank_mask:0xf
	s_nop 1
	v_readlane_b32 s28, v41, 63
	s_nop 1
	v_div_scale_f32 v48, s[30:31], s28, s28, v47
	v_rcp_f32_e32 v49, v48
	s_nop 0
	v_fma_f32 v50, -v48, v49, 1.0
	v_fmac_f32_e32 v49, v50, v49
	v_mov_b32_e32 v50, s28
	v_div_scale_f32 v50, vcc, s32, v50, s32
	v_mul_f32_e32 v51, v50, v49
	v_fma_f32 v52, -v48, v51, v50
	v_fmac_f32_e32 v51, v52, v49
	v_fma_f32 v48, -v48, v51, v50
	v_div_fmas_f32 v48, v48, v49, v51
	v_div_fixup_f32 v48, v48, s28, v47
	v_cmp_gt_f32_e64 vcc, s28, 0
	v_writelane_b32 v40, s28, 20
	s_nop 0
	v_cndmask_b32_e32 v48, 0, v48, vcc
	v_fmaak_f32 v49, v18, v48, 0x4b400000
	v_fmaak_f32 v50, v19, v48, 0x4b400000
	v_fmaak_f32 v51, v20, v48, 0x4b400000
	v_fmaak_f32 v52, v21, v48, 0x4b400000
	v_perm_b32 v49, v50, v49, s33
	v_perm_b32 v51, v52, v51, s34
	v_or_b32_e32 v49, v49, v51
	ds_write_b32 v38, v49 offset:4096
	v_fmaak_f32 v41, v22, v48, 0x4b400000
	v_fmaak_f32 v42, v23, v48, 0x4b400000
	v_fmaak_f32 v43, v24, v48, 0x4b400000
	v_fmaak_f32 v44, v25, v48, 0x4b400000
	v_perm_b32 v41, v42, v41, s33
	v_perm_b32 v43, v44, v43, s34
	v_or_b32_e32 v41, v41, v43
	ds_write_b32 v38, v41 offset:4100
	v_fmaak_f32 v49, v26, v48, 0x4b400000
	v_fmaak_f32 v50, v27, v48, 0x4b400000
	v_fmaak_f32 v51, v28, v48, 0x4b400000
	v_fmaak_f32 v52, v29, v48, 0x4b400000
	v_perm_b32 v49, v50, v49, s33
	v_perm_b32 v51, v52, v51, s34
	v_or_b32_e32 v49, v49, v51
	ds_write_b32 v38, v49 offset:4104
	v_fmaak_f32 v41, v30, v48, 0x4b400000
	v_fmaak_f32 v42, v31, v48, 0x4b400000
	v_fmaak_f32 v43, v32, v48, 0x4b400000
	v_fmaak_f32 v44, v33, v48, 0x4b400000
	v_perm_b32 v41, v42, v41, s33
	v_perm_b32 v43, v44, v43, s34
	v_or_b32_e32 v41, v41, v43
	ds_write_b32 v38, v41 offset:4108
	s_waitcnt vmcnt(0)
	ds_read_b128 v[18:21], v38 offset:0
	ds_read_b128 v[22:25], v38 offset:1024
	ds_read_b128 v[26:29], v38 offset:2048
	ds_read_b128 v[30:33], v38 offset:3072
	s_waitcnt lgkmcnt(0)
	s_barrier
	s_mov_b32 m0, s35
	s_nop 0
	global_load_lds_dwordx4 v34, s[16:17] nt
	global_load_lds_dwordx4 v34, s[16:17] offset:1024 nt
	global_load_lds_dwordx4 v34, s[16:17] offset:2048 nt
	global_load_lds_dwordx4 v35, s[16:17] offset:3072 nt
	s_add_u32 s16, s16, 0x7d00
	s_addc_u32 s17, s17, 0
	v_cndmask_b32_e64 v30, 0, v30, s[18:19]
	v_cndmask_b32_e64 v31, 0, v31, s[18:19]
	v_cndmask_b32_e64 v32, 0, v32, s[18:19]
	v_cndmask_b32_e64 v33, 0, v33, s[18:19]
	v_max3_f32 v41, |v18|, |v19|, |v20|
	v_max3_f32 v42, |v21|, |v22|, |v23|
	v_max3_f32 v43, |v24|, |v25|, |v26|
	v_max3_f32 v44, |v27|, |v28|, |v29|
	v_max3_f32 v48, |v30|, |v31|, |v32|
	v_max3_f32 v41, v41, v42, |v33|
	v_max3_f32 v43, v43, v44, v48
	v_max_f32_e32 v41, v41, v43
	v_pk_add_f32 v[2:3], v[2:3], v[18:19]
	v_pk_add_f32 v[4:5], v[4:5], v[20:21]
	v_max_f32_dpp v41, v41, v41 quad_perm:[1,0,3,2] row_mask:0xf bank_mask:0xf
	v_pk_add_f32 v[6:7], v[6:7], v[22:23]
	v_pk_add_f32 v[8:9], v[8:9], v[24:25]
	v_max_f32_dpp v41, v41, v41 quad_perm:[2,3,0,1] row_mask:0xf bank_mask:0xf
	v_pk_add_f32 v[10:11], v[10:11], v[26:27]
	v_pk_add_f32 v[12:13], v[12:13], v[28:29]
	v_max_f32_dpp v41, v41, v41 row_half_mirror row_mask:0xf bank_mask:0xf
	v_pk_add_f32 v[14:15], v[14:15], v[30:31]
	v_pk_add_f32 v[16:17], v[16:17], v[32:33]
	v_max_f32_dpp v41, v41, v41 row_mirror row_mask:0xf bank_mask:0xf
	s_nop 1
	v_max_f32_dpp v41, v41, v41 row_bcast:15 row_mask:0xa bank_mask:0xf
	s_nop 1
	v_max_f32_dpp v41, v41, v41 row_bcast:31 row_mask:0xc bank_mask:0xf
	s_nop 1
	v_readlane_b32 s28, v41, 63
	s_nop 1
	v_div_scale_f32 v48, s[30:31], s28, s28, v47
	v_rcp_f32_e32 v49, v48
	s_nop 0
	v_fma_f32 v50, -v48, v49, 1.0
	v_fmac_f32_e32 v49, v50, v49
	v_mov_b32_e32 v50, s28
	v_div_scale_f32 v50, vcc, s32, v50, s32
	v_mul_f32_e32 v51, v50, v49
	v_fma_f32 v52, -v48, v51, v50
	v_fmac_f32_e32 v51, v52, v49
	v_fma_f32 v48, -v48, v51, v50
	v_div_fmas_f32 v48, v48, v49, v51
	v_div_fixup_f32 v48, v48, s28, v47
	v_cmp_gt_f32_e64 vcc, s28, 0
	v_writelane_b32 v40, s28, 21
	s_nop 0
	v_cndmask_b32_e32 v48, 0, v48, vcc
	v_fmaak_f32 v49, v18, v48, 0x4b400000
	v_fmaak_f32 v50, v19, v48, 0x4b400000
	v_fmaak_f32 v51, v20, v48, 0x4b400000
	v_fmaak_f32 v52, v21, v48, 0x4b400000
	v_perm_b32 v49, v50, v49, s33
	v_perm_b32 v51, v52, v51, s34
	v_or_b32_e32 v49, v49, v51
	ds_write_b32 v38, v49 offset:5120
	v_fmaak_f32 v41, v22, v48, 0x4b400000
	v_fmaak_f32 v42, v23, v48, 0x4b400000
	v_fmaak_f32 v43, v24, v48, 0x4b400000
	v_fmaak_f32 v44, v25, v48, 0x4b400000
	v_perm_b32 v41, v42, v41, s33
	v_perm_b32 v43, v44, v43, s34
	v_or_b32_e32 v41, v41, v43
	ds_write_b32 v38, v41 offset:5124
	v_fmaak_f32 v49, v26, v48, 0x4b400000
	v_fmaak_f32 v50, v27, v48, 0x4b400000
	v_fmaak_f32 v51, v28, v48, 0x4b400000
	v_fmaak_f32 v52, v29, v48, 0x4b400000
	v_perm_b32 v49, v50, v49, s33
	v_perm_b32 v51, v52, v51, s34
	v_or_b32_e32 v49, v49, v51
	ds_write_b32 v38, v49 offset:5128
	v_fmaak_f32 v41, v30, v48, 0x4b400000
	v_fmaak_f32 v42, v31, v48, 0x4b400000
	v_fmaak_f32 v43, v32, v48, 0x4b400000
	v_fmaak_f32 v44, v33, v48, 0x4b400000
	v_perm_b32 v41, v42, v41, s33
	v_perm_b32 v43, v44, v43, s34
	v_or_b32_e32 v41, v41, v43
	ds_write_b32 v38, v41 offset:5132
	s_waitcnt vmcnt(0)
	ds_read_b128 v[18:21], v38 offset:0
	ds_read_b128 v[22:25], v38 offset:1024
	ds_read_b128 v[26:29], v38 offset:2048
	ds_read_b128 v[30:33], v38 offset:3072
	s_waitcnt lgkmcnt(0)
	s_barrier
	s_mov_b32 m0, s35
	s_nop 0
	global_load_lds_dwordx4 v34, s[16:17] nt
	global_load_lds_dwordx4 v34, s[16:17] offset:1024 nt
	global_load_lds_dwordx4 v34, s[16:17] offset:2048 nt
	global_load_lds_dwordx4 v35, s[16:17] offset:3072 nt
	s_add_u32 s16, s16, 0x7d00
	s_addc_u32 s17, s17, 0
	v_cndmask_b32_e64 v30, 0, v30, s[18:19]
	v_cndmask_b32_e64 v31, 0, v31, s[18:19]
	v_cndmask_b32_e64 v32, 0, v32, s[18:19]
	v_cndmask_b32_e64 v33, 0, v33, s[18:19]
	v_max3_f32 v41, |v18|, |v19|, |v20|
	v_max3_f32 v42, |v21|, |v22|, |v23|
	v_max3_f32 v43, |v24|, |v25|, |v26|
	v_max3_f32 v44, |v27|, |v28|, |v29|
	v_max3_f32 v48, |v30|, |v31|, |v32|
	v_max3_f32 v41, v41, v42, |v33|
	v_max3_f32 v43, v43, v44, v48
	v_max_f32_e32 v41, v41, v43
	v_pk_add_f32 v[2:3], v[2:3], v[18:19]
	v_pk_add_f32 v[4:5], v[4:5], v[20:21]
	v_max_f32_dpp v41, v41, v41 quad_perm:[1,0,3,2] row_mask:0xf bank_mask:0xf
	v_pk_add_f32 v[6:7], v[6:7], v[22:23]
	v_pk_add_f32 v[8:9], v[8:9], v[24:25]
	v_max_f32_dpp v41, v41, v41 quad_perm:[2,3,0,1] row_mask:0xf bank_mask:0xf
	v_pk_add_f32 v[10:11], v[10:11], v[26:27]
	v_pk_add_f32 v[12:13], v[12:13], v[28:29]
	v_max_f32_dpp v41, v41, v41 row_half_mirror row_mask:0xf bank_mask:0xf
	v_pk_add_f32 v[14:15], v[14:15], v[30:31]
	v_pk_add_f32 v[16:17], v[16:17], v[32:33]
	v_max_f32_dpp v41, v41, v41 row_mirror row_mask:0xf bank_mask:0xf
	s_nop 1
	v_max_f32_dpp v41, v41, v41 row_bcast:15 row_mask:0xa bank_mask:0xf
	s_nop 1
	v_max_f32_dpp v41, v41, v41 row_bcast:31 row_mask:0xc bank_mask:0xf
	s_nop 1
	v_readlane_b32 s28, v41, 63
	s_nop 1
	v_div_scale_f32 v48, s[30:31], s28, s28, v47
	v_rcp_f32_e32 v49, v48
	s_nop 0
	v_fma_f32 v50, -v48, v49, 1.0
	v_fmac_f32_e32 v49, v50, v49
	v_mov_b32_e32 v50, s28
	v_div_scale_f32 v50, vcc, s32, v50, s32
	v_mul_f32_e32 v51, v50, v49
	v_fma_f32 v52, -v48, v51, v50
	v_fmac_f32_e32 v51, v52, v49
	v_fma_f32 v48, -v48, v51, v50
	v_div_fmas_f32 v48, v48, v49, v51
	v_div_fixup_f32 v48, v48, s28, v47
	v_cmp_gt_f32_e64 vcc, s28, 0
	v_writelane_b32 v40, s28, 22
	s_nop 0
	v_cndmask_b32_e32 v48, 0, v48, vcc
	v_fmaak_f32 v49, v18, v48, 0x4b400000
	v_fmaak_f32 v50, v19, v48, 0x4b400000
	v_fmaak_f32 v51, v20, v48, 0x4b400000
	v_fmaak_f32 v52, v21, v48, 0x4b400000
	v_perm_b32 v49, v50, v49, s33
	v_perm_b32 v51, v52, v51, s34
	v_or_b32_e32 v49, v49, v51
	ds_write_b32 v38, v49 offset:6144
	v_fmaak_f32 v41, v22, v48, 0x4b400000
	v_fmaak_f32 v42, v23, v48, 0x4b400000
	v_fmaak_f32 v43, v24, v48, 0x4b400000
	v_fmaak_f32 v44, v25, v48, 0x4b400000
	v_perm_b32 v41, v42, v41, s33
	v_perm_b32 v43, v44, v43, s34
	v_or_b32_e32 v41, v41, v43
	ds_write_b32 v38, v41 offset:6148
	v_fmaak_f32 v49, v26, v48, 0x4b400000
	v_fmaak_f32 v50, v27, v48, 0x4b400000
	v_fmaak_f32 v51, v28, v48, 0x4b400000
	v_fmaak_f32 v52, v29, v48, 0x4b400000
	v_perm_b32 v49, v50, v49, s33
	v_perm_b32 v51, v52, v51, s34
	v_or_b32_e32 v49, v49, v51
	ds_write_b32 v38, v49 offset:6152
	v_fmaak_f32 v41, v30, v48, 0x4b400000
	v_fmaak_f32 v42, v31, v48, 0x4b400000
	v_fmaak_f32 v43, v32, v48, 0x4b400000
	v_fmaak_f32 v44, v33, v48, 0x4b400000
	v_perm_b32 v41, v42, v41, s33
	v_perm_b32 v43, v44, v43, s34
	v_or_b32_e32 v41, v41, v43
	ds_write_b32 v38, v41 offset:6156
	s_waitcnt vmcnt(0)
	ds_read_b128 v[18:21], v38 offset:0
	ds_read_b128 v[22:25], v38 offset:1024
	ds_read_b128 v[26:29], v38 offset:2048
	ds_read_b128 v[30:33], v38 offset:3072
	s_waitcnt lgkmcnt(0)
	s_cmp_eq_u32 s29, 1
	s_cbranch_scc0 .Lk1_nodma24
	s_mov_b32 m0, s35
	s_nop 0
	global_load_lds_dwordx4 v34, s[16:17] nt
	global_load_lds_dwordx4 v34, s[16:17] offset:1024 nt
	global_load_lds_dwordx4 v34, s[16:17] offset:2048 nt
	global_load_lds_dwordx4 v35, s[16:17] offset:3072 nt
	s_add_u32 s16, s16, 0x7d00
	s_addc_u32 s17, s17, 0
.Lk1_nodma24:
	v_cndmask_b32_e64 v30, 0, v30, s[18:19]
	v_cndmask_b32_e64 v31, 0, v31, s[18:19]
	v_cndmask_b32_e64 v32, 0, v32, s[18:19]
	v_cndmask_b32_e64 v33, 0, v33, s[18:19]
	v_max3_f32 v41, |v18|, |v19|, |v20|
	v_max3_f32 v42, |v21|, |v22|, |v23|
	v_max3_f32 v43, |v24|, |v25|, |v26|
	v_max3_f32 v44, |v27|, |v28|, |v29|
	v_max3_f32 v48, |v30|, |v31|, |v32|
	v_max3_f32 v41, v41, v42, |v33|
	v_max3_f32 v43, v43, v44, v48
	v_max_f32_e32 v41, v41, v43
	v_pk_add_f32 v[2:3], v[2:3], v[18:19]
	v_pk_add_f32 v[4:5], v[4:5], v[20:21]
	v_max_f32_dpp v41, v41, v41 quad_perm:[1,0,3,2] row_mask:0xf bank_mask:0xf
	v_pk_add_f32 v[6:7], v[6:7], v[22:23]
	v_pk_add_f32 v[8:9], v[8:9], v[24:25]
	v_max_f32_dpp v41, v41, v41 quad_perm:[2,3,0,1] row_mask:0xf bank_mask:0xf
	v_pk_add_f32 v[10:11], v[10:11], v[26:27]
	v_pk_add_f32 v[12:13], v[12:13], v[28:29]
	v_max_f32_dpp v41, v41, v41 row_half_mirror row_mask:0xf bank_mask:0xf
	v_pk_add_f32 v[14:15], v[14:15], v[30:31]
	v_pk_add_f32 v[16:17], v[16:17], v[32:33]
	v_max_f32_dpp v41, v41, v41 row_mirror row_mask:0xf bank_mask:0xf
	s_nop 1
	v_max_f32_dpp v41, v41, v41 row_bcast:15 row_mask:0xa bank_mask:0xf
	s_nop 1
	v_max_f32_dpp v41, v41, v41 row_bcast:31 row_mask:0xc bank_mask:0xf
	s_nop 1
	v_readlane_b32 s28, v41, 63
	s_nop 1
	v_div_scale_f32 v48, s[30:31], s28, s28, v47
	v_rcp_f32_e32 v49, v48
	s_nop 0
	v_fma_f32 v50, -v48, v49, 1.0
	v_fmac_f32_e32 v49, v50, v49
	v_mov_b32_e32 v50, s28
	v_div_scale_f32 v50, vcc, s32, v50, s32
	v_mul_f32_e32 v51, v50, v49
	v_fma_f32 v52, -v48, v51, v50
	v_fmac_f32_e32 v51, v52, v49
	v_fma_f32 v48, -v48, v51, v50
	v_div_fmas_f32 v48, v48, v49, v51
	v_div_fixup_f32 v48, v48, s28, v47
	v_cmp_gt_f32_e64 vcc, s28, 0
	v_writelane_b32 v40, s28, 23
	s_nop 0
	v_cndmask_b32_e32 v48, 0, v48, vcc
	v_fmaak_f32 v49, v18, v48, 0x4b400000
	v_fmaak_f32 v50, v19, v48, 0x4b400000
	v_fmaak_f32 v51, v20, v48, 0x4b400000
	v_fmaak_f32 v52, v21, v48, 0x4b400000
	v_perm_b32 v49, v50, v49, s33
	v_perm_b32 v51, v52, v51, s34
	v_or_b32_e32 v49, v49, v51
	ds_write_b32 v38, v49 offset:7168
	v_fmaak_f32 v41, v22, v48, 0x4b400000
	v_fmaak_f32 v42, v23, v48, 0x4b400000
	v_fmaak_f32 v43, v24, v48, 0x4b400000
	v_fmaak_f32 v44, v25, v48, 0x4b400000
	v_perm_b32 v41, v42, v41, s33
	v_perm_b32 v43, v44, v43, s34
	v_or_b32_e32 v41, v41, v43
	ds_write_b32 v38, v41 offset:7172
	v_fmaak_f32 v49, v26, v48, 0x4b400000
	v_fmaak_f32 v50, v27, v48, 0x4b400000
	v_fmaak_f32 v51, v28, v48, 0x4b400000
	v_fmaak_f32 v52, v29, v48, 0x4b400000
	v_perm_b32 v49, v50, v49, s33
	v_perm_b32 v51, v52, v51, s34
	v_or_b32_e32 v49, v49, v51
	ds_write_b32 v38, v49 offset:7176
	v_fmaak_f32 v41, v30, v48, 0x4b400000
	v_fmaak_f32 v42, v31, v48, 0x4b400000
	v_fmaak_f32 v43, v32, v48, 0x4b400000
	v_fmaak_f32 v44, v33, v48, 0x4b400000
	v_perm_b32 v41, v42, v41, s33
	v_perm_b32 v43, v44, v43, s34
	v_or_b32_e32 v41, v41, v43
	ds_write_b32 v38, v41 offset:7180
	s_cmp_eq_u32 s29, 1
	s_cbranch_scc0 .Lk1_flush
	s_waitcnt vmcnt(0)
	ds_read_b128 v[18:21], v38 offset:0
	ds_read_b128 v[22:25], v38 offset:1024
	ds_read_b128 v[26:29], v38 offset:2048
	ds_read_b128 v[30:33], v38 offset:3072
	s_waitcnt lgkmcnt(0)
	v_cndmask_b32_e64 v30, 0, v30, s[18:19]
	v_cndmask_b32_e64 v31, 0, v31, s[18:19]
	v_cndmask_b32_e64 v32, 0, v32, s[18:19]
	v_cndmask_b32_e64 v33, 0, v33, s[18:19]
	v_max3_f32 v41, |v18|, |v19|, |v20|
	v_max3_f32 v42, |v21|, |v22|, |v23|
	v_max3_f32 v43, |v24|, |v25|, |v26|
	v_max3_f32 v44, |v27|, |v28|, |v29|
	v_max3_f32 v48, |v30|, |v31|, |v32|
	v_max3_f32 v41, v41, v42, |v33|
	v_max3_f32 v43, v43, v44, v48
	v_max_f32_e32 v41, v41, v43
	v_pk_add_f32 v[2:3], v[2:3], v[18:19]
	v_pk_add_f32 v[4:5], v[4:5], v[20:21]
	v_max_f32_dpp v41, v41, v41 quad_perm:[1,0,3,2] row_mask:0xf bank_mask:0xf
	v_pk_add_f32 v[6:7], v[6:7], v[22:23]
	v_pk_add_f32 v[8:9], v[8:9], v[24:25]
	v_max_f32_dpp v41, v41, v41 quad_perm:[2,3,0,1] row_mask:0xf bank_mask:0xf
	v_pk_add_f32 v[10:11], v[10:11], v[26:27]
	v_pk_add_f32 v[12:13], v[12:13], v[28:29]
	v_max_f32_dpp v41, v41, v41 row_half_mirror row_mask:0xf bank_mask:0xf
	v_pk_add_f32 v[14:15], v[14:15], v[30:31]
	v_pk_add_f32 v[16:17], v[16:17], v[32:33]
	v_max_f32_dpp v41, v41, v41 row_mirror row_mask:0xf bank_mask:0xf
	s_nop 1
	v_max_f32_dpp v41, v41, v41 row_bcast:15 row_mask:0xa bank_mask:0xf
	s_nop 1
	v_max_f32_dpp v41, v41, v41 row_bcast:31 row_mask:0xc bank_mask:0xf
	s_nop 1
	v_readlane_b32 s28, v41, 63
	s_nop 1
	v_div_scale_f32 v48, s[30:31], s28, s28, v47
	v_rcp_f32_e32 v49, v48
	s_nop 0
	v_fma_f32 v50, -v48, v49, 1.0
	v_fmac_f32_e32 v49, v50, v49
	v_mov_b32_e32 v50, s28
	v_div_scale_f32 v50, vcc, s32, v50, s32
	v_mul_f32_e32 v51, v50, v49
	v_fma_f32 v52, -v48, v51, v50
	v_fmac_f32_e32 v51, v52, v49
	v_fma_f32 v48, -v48, v51, v50
	v_div_fmas_f32 v48, v48, v49, v51
	v_div_fixup_f32 v48, v48, s28, v47
	v_cmp_gt_f32_e64 vcc, s28, 0
	v_writelane_b32 v40, s28, 24
	s_nop 0
	v_cndmask_b32_e32 v48, 0, v48, vcc
	v_fmaak_f32 v49, v18, v48, 0x4b400000
	v_fmaak_f32 v50, v19, v48, 0x4b400000
	v_fmaak_f32 v51, v20, v48, 0x4b400000
	v_fmaak_f32 v52, v21, v48, 0x4b400000
	v_perm_b32 v49, v50, v49, s33
	v_perm_b32 v51, v52, v51, s34
	v_or_b32_e32 v49, v49, v51
	s_add_u32 s20, s20, 0x6000
	s_addc_u32 s21, s21, 0
	s_add_u32 s22, s22, 0x6000
	s_addc_u32 s23, s23, 0
	s_add_u32 s24, s24, 0x6000
	s_addc_u32 s25, s25, 0
	s_add_u32 s26, s26, 0x6000
	s_addc_u32 s27, s27, 0
	global_store_dword v39, v49, s[20:21]
	v_fmaak_f32 v41, v22, v48, 0x4b400000
	v_fmaak_f32 v42, v23, v48, 0x4b400000
	v_fmaak_f32 v43, v24, v48, 0x4b400000
	v_fmaak_f32 v44, v25, v48, 0x4b400000
	v_perm_b32 v41, v42, v41, s33
	v_perm_b32 v43, v44, v43, s34
	v_or_b32_e32 v41, v41, v43
	global_store_dword v39, v41, s[22:23]
	v_fmaak_f32 v49, v26, v48, 0x4b400000
	v_fmaak_f32 v50, v27, v48, 0x4b400000
	v_fmaak_f32 v51, v28, v48, 0x4b400000
	v_fmaak_f32 v52, v29, v48, 0x4b400000
	v_perm_b32 v49, v50, v49, s33
	v_perm_b32 v51, v52, v51, s34
	v_or_b32_e32 v49, v49, v51
	global_store_dword v39, v49, s[24:25]
	v_fmaak_f32 v41, v30, v48, 0x4b400000
	v_fmaak_f32 v42, v31, v48, 0x4b400000
	v_fmaak_f32 v43, v32, v48, 0x4b400000
	v_fmaak_f32 v44, v33, v48, 0x4b400000
	v_perm_b32 v41, v42, v41, s33
	v_perm_b32 v43, v44, v43, s34
	v_or_b32_e32 v41, v41, v43
	global_store_dword v39, v41, s[26:27]
.Lk1_flush:
	s_add_u32 s20, s40, 0x0
	s_addc_u32 s21, s41, 0
	s_add_u32 s22, s20, 0x186a000
	s_addc_u32 s23, s21, 0
	s_add_u32 s24, s22, 0x186a000
	s_addc_u32 s25, s23, 0
	s_add_u32 s26, s24, 0x186a000
	s_addc_u32 s27, s25, 0
	global_store_dword v39, v56, s[20:21] sc1
	global_store_dword v39, v57, s[22:23] sc1
	global_store_dword v39, v58, s[24:25] sc1
	global_store_dword v39, v59, s[26:27] sc1
	global_store_dword v39, v60, s[20:21] offset:1024 sc1
	global_store_dword v39, v61, s[22:23] offset:1024 sc1
	global_store_dword v39, v62, s[24:25] offset:1024 sc1
	global_store_dword v39, v63, s[26:27] offset:1024 sc1
	global_store_dword v39, v64, s[20:21] offset:2048 sc1
	global_store_dword v39, v65, s[22:23] offset:2048 sc1
	global_store_dword v39, v66, s[24:25] offset:2048 sc1
	global_store_dword v39, v67, s[26:27] offset:2048 sc1
	global_store_dword v39, v68, s[20:21] offset:3072 sc1
	global_store_dword v39, v69, s[22:23] offset:3072 sc1
	global_store_dword v39, v70, s[24:25] offset:3072 sc1
	global_store_dword v39, v71, s[26:27] offset:3072 sc1
	s_add_u32 s20, s20, 0x1000
	s_addc_u32 s21, s21, 0
	s_add_u32 s22, s22, 0x1000
	s_addc_u32 s23, s23, 0
	s_add_u32 s24, s24, 0x1000
	s_addc_u32 s25, s25, 0
	s_add_u32 s26, s26, 0x1000
	s_addc_u32 s27, s27, 0
	global_store_dword v39, v72, s[20:21] sc1
	global_store_dword v39, v73, s[22:23] sc1
	global_store_dword v39, v74, s[24:25] sc1
	global_store_dword v39, v75, s[26:27] sc1
	global_store_dword v39, v76, s[20:21] offset:1024 sc1
	global_store_dword v39, v77, s[22:23] offset:1024 sc1
	global_store_dword v39, v78, s[24:25] offset:1024 sc1
	global_store_dword v39, v79, s[26:27] offset:1024 sc1
	global_store_dword v39, v80, s[20:21] offset:2048 sc1
	global_store_dword v39, v81, s[22:23] offset:2048 sc1
	global_store_dword v39, v82, s[24:25] offset:2048 sc1
	global_store_dword v39, v83, s[26:27] offset:2048 sc1
	global_store_dword v39, v84, s[20:21] offset:3072 sc1
	global_store_dword v39, v85, s[22:23] offset:3072 sc1
	global_store_dword v39, v86, s[24:25] offset:3072 sc1
	global_store_dword v39, v87, s[26:27] offset:3072 sc1
	s_add_u32 s20, s20, 0x1000
	s_addc_u32 s21, s21, 0
	s_add_u32 s22, s22, 0x1000
	s_addc_u32 s23, s23, 0
	s_add_u32 s24, s24, 0x1000
	s_addc_u32 s25, s25, 0
	s_add_u32 s26, s26, 0x1000
	s_addc_u32 s27, s27, 0
	global_store_dword v39, v88, s[20:21] sc1
	global_store_dword v39, v89, s[22:23] sc1
	global_store_dword v39, v90, s[24:25] sc1
	global_store_dword v39, v91, s[26:27] sc1
	global_store_dword v39, v92, s[20:21] offset:1024 sc1
	global_store_dword v39, v93, s[22:23] offset:1024 sc1
	global_store_dword v39, v94, s[24:25] offset:1024 sc1
	global_store_dword v39, v95, s[26:27] offset:1024 sc1
	global_store_dword v39, v96, s[20:21] offset:2048 sc1
	global_store_dword v39, v97, s[22:23] offset:2048 sc1
	global_store_dword v39, v98, s[24:25] offset:2048 sc1
	global_store_dword v39, v99, s[26:27] offset:2048 sc1
	global_store_dword v39, v100, s[20:21] offset:3072 sc1
	global_store_dword v39, v101, s[22:23] offset:3072 sc1
	global_store_dword v39, v102, s[24:25] offset:3072 sc1
	global_store_dword v39, v103, s[26:27] offset:3072 sc1
	s_add_u32 s20, s20, 0x1000
	s_addc_u32 s21, s21, 0
	s_add_u32 s22, s22, 0x1000
	s_addc_u32 s23, s23, 0
	s_add_u32 s24, s24, 0x1000
	s_addc_u32 s25, s25, 0
	s_add_u32 s26, s26, 0x1000
	s_addc_u32 s27, s27, 0
	global_store_dword v39, v104, s[20:21] sc1
	global_store_dword v39, v105, s[22:23] sc1
	global_store_dword v39, v106, s[24:25] sc1
	global_store_dword v39, v107, s[26:27] sc1
	global_store_dword v39, v108, s[20:21] offset:1024 sc1
	global_store_dword v39, v109, s[22:23] offset:1024 sc1
	global_store_dword v39, v110, s[24:25] offset:1024 sc1
	global_store_dword v39, v111, s[26:27] offset:1024 sc1
	global_store_dword v39, v112, s[20:21] offset:2048 sc1
	global_store_dword v39, v113, s[22:23] offset:2048 sc1
	global_store_dword v39, v114, s[24:25] offset:2048 sc1
	global_store_dword v39, v115, s[26:27] offset:2048 sc1
	global_store_dword v39, v116, s[20:21] offset:3072 sc1
	global_store_dword v39, v117, s[22:23] offset:3072 sc1
	global_store_dword v39, v118, s[24:25] offset:3072 sc1
	global_store_dword v39, v119, s[26:27] offset:3072 sc1
	s_add_u32 s20, s20, 0x1000
	s_addc_u32 s21, s21, 0
	s_add_u32 s22, s22, 0x1000
	s_addc_u32 s23, s23, 0
	s_add_u32 s24, s24, 0x1000
	s_addc_u32 s25, s25, 0
	s_add_u32 s26, s26, 0x1000
	s_addc_u32 s27, s27, 0
	global_store_dword v39, v120, s[20:21] sc1
	global_store_dword v39, v121, s[22:23] sc1
	global_store_dword v39, v122, s[24:25] sc1
	global_store_dword v39, v123, s[26:27] sc1
	global_store_dword v39, v124, s[20:21] offset:1024 sc1
	global_store_dword v39, v125, s[22:23] offset:1024 sc1
	global_store_dword v39, v126, s[24:25] offset:1024 sc1
	global_store_dword v39, v127, s[26:27] offset:1024 sc1
	global_store_dword v39, v36, s[20:21] offset:2048 sc1
	global_store_dword v39, v37, s[22:23] offset:2048 sc1
	global_store_dword v39, v45, s[24:25] offset:2048 sc1
	global_store_dword v39, v46, s[26:27] offset:2048 sc1
	global_store_dword v39, v53, s[20:21] offset:3072 sc1
	global_store_dword v39, v54, s[22:23] offset:3072 sc1
	global_store_dword v39, v55, s[24:25] offset:3072 sc1
	global_store_dword v39, v1, s[26:27] offset:3072 sc1
	s_add_u32 s20, s20, 0x1000
	s_addc_u32 s21, s21, 0
	s_add_u32 s22, s22, 0x1000
	s_addc_u32 s23, s23, 0
	s_add_u32 s24, s24, 0x1000
	s_addc_u32 s25, s25, 0
	s_add_u32 s26, s26, 0x1000
	s_addc_u32 s27, s27, 0
	ds_read_b128 v[56:59], v38 offset:4096
	ds_read_b128 v[60:63], v38 offset:5120
	ds_read_b128 v[64:67], v38 offset:6144
	ds_read_b128 v[68:71], v38 offset:7168
	s_waitcnt lgkmcnt(0)
	global_store_dword v39, v56, s[20:21] sc1
	global_store_dword v39, v57, s[22:23] sc1
	global_store_dword v39, v58, s[24:25] sc1
	global_store_dword v39, v59, s[26:27] sc1
	global_store_dword v39, v60, s[20:21] offset:1024 sc1
	global_store_dword v39, v61, s[22:23] offset:1024 sc1
	global_store_dword v39, v62, s[24:25] offset:1024 sc1
	global_store_dword v39, v63, s[26:27] offset:1024 sc1
	global_store_dword v39, v64, s[20:21] offset:2048 sc1
	global_store_dword v39, v65, s[22:23] offset:2048 sc1
	global_store_dword v39, v66, s[24:25] offset:2048 sc1
	global_store_dword v39, v67, s[26:27] offset:2048 sc1
	global_store_dword v39, v68, s[20:21] offset:3072 sc1
	global_store_dword v39, v69, s[22:23] offset:3072 sc1
	global_store_dword v39, v70, s[24:25] offset:3072 sc1
	global_store_dword v39, v71, s[26:27] offset:3072 sc1
	v_mul_f32_e32 v40, 0x3c010204, v40
	v_and_b32_e32 v42, 63, v0
	v_lshlrev_b32_e32 v41, 5, v42
	s_add_u32 s15, s12, s14
	s_lshl_b32 s15, s15, 2
	s_add_u32 s8, s8, s15
	s_addc_u32 s9, s9, 0
	s_add_u32 s15, s29, 24
	v_cmp_gt_u32_e32 vcc, s15, v42
	s_and_saveexec_b64 s[38:39], vcc
	global_store_dword v41, v40, s[8:9]
	s_mov_b64 exec, s[38:39]
	s_lshl_b32 s15, s14, 12
	v_add_u32_e32 v41, s15, v34
	s_barrier
	ds_write_b128 v41, v[2:5]
	ds_write_b128 v41, v[6:9] offset:1024
	ds_write_b128 v41, v[10:13] offset:2048
	ds_write_b128 v41, v[14:17] offset:3072
	s_waitcnt lgkmcnt(0)
	s_barrier
	s_movk_i32 s15, 0x100
	v_cmp_gt_u32_e32 vcc, s15, v0
	s_and_saveexec_b64 s[38:39], vcc
	s_cbranch_execz .Lk1_end
	v_lshlrev_b32_e32 v16, 4, v0
	ds_read_b128 v[2:5], v16
	ds_read_b128 v[18:21], v16 offset:4096
	ds_read_b128 v[22:25], v16 offset:8192
	ds_read_b128 v[26:29], v16 offset:12288
	ds_read_b128 v[30:33], v16 offset:16384
	ds_read_b128 v[34:37], v16 offset:20480
	ds_read_b128 v[38:41], v16 offset:24576
	ds_read_b128 v[42:45], v16 offset:28672
	s_waitcnt lgkmcnt(6)
	v_pk_add_f32 v[2:3], v[2:3], v[18:19]
	v_pk_add_f32 v[4:5], v[4:5], v[20:21]
	s_waitcnt lgkmcnt(5)
	v_pk_add_f32 v[2:3], v[2:3], v[22:23]
	v_pk_add_f32 v[4:5], v[4:5], v[24:25]
	s_waitcnt lgkmcnt(4)
	v_pk_add_f32 v[2:3], v[2:3], v[26:27]
	v_pk_add_f32 v[4:5], v[4:5], v[28:29]
	s_waitcnt lgkmcnt(3)
	v_pk_add_f32 v[2:3], v[2:3], v[30:31]
	v_pk_add_f32 v[4:5], v[4:5], v[32:33]
	s_waitcnt lgkmcnt(2)
	v_pk_add_f32 v[2:3], v[2:3], v[34:35]
	v_pk_add_f32 v[4:5], v[4:5], v[36:37]
	s_waitcnt lgkmcnt(1)
	v_pk_add_f32 v[2:3], v[2:3], v[38:39]
	v_pk_add_f32 v[4:5], v[4:5], v[40:41]
	s_waitcnt lgkmcnt(0)
	v_pk_add_f32 v[2:3], v[2:3], v[42:43]
	v_pk_add_f32 v[4:5], v[4:5], v[44:45]
	s_lshl_b32 s15, s2, 12
	s_add_u32 s10, s10, s15
	s_addc_u32 s11, s11, 0
	global_store_dwordx4 v16, v[2:5], s[10:11]
